# prologue weight transposes: an item's 8 RMSNorm-gain values loaded once with its tile loads instead of 16 dependent little loads over four sub-blocks
# baseline (speedup 1.0000x reference)
.LBB0_64:
	s_lshr_b32 s24, s4, 7
	s_waitcnt vmcnt(0)
	v_cvt_f32_u32_e32 v0, s24
	s_sub_i32 s25, 0, s24
	s_xor_b64 s[34:35], s[2:3], -1
	s_ashr_i32 s2, s58, 2
	v_rcp_iflag_f32_e32 v0, v0
	s_abs_i32 s3, s2
	v_mul_f32_e32 v0, 0x4f7ffffe, v0
	v_cvt_u32_f32_e32 v0, v0
	s_nop 0
	v_readfirstlane_b32 s36, v0
	s_mul_i32 s25, s25, s36
	s_mul_hi_u32 s25, s36, s25
	s_add_i32 s36, s36, s25
	s_mul_hi_u32 s25, s3, s36
	s_mul_i32 s36, s25, s24
	s_sub_i32 s3, s3, s36
	s_add_i32 s37, s25, 1
	s_sub_i32 s36, s3, s24
	s_cmp_ge_u32 s3, s24
	s_cselect_b32 s25, s37, s25
	s_cselect_b32 s3, s36, s3
	s_add_i32 s36, s25, 1
	s_cmp_ge_u32 s3, s24
	s_cselect_b32 s3, s36, s25
	s_ashr_i32 s59, s58, 31
	s_xor_b32 s3, s3, s59
	s_sub_i32 s3, s3, s59
	s_mul_i32 s24, s3, s24
	s_lshl_b32 s3, s3, 6
	v_or_b32_e32 v0, s3, v136
	s_ashr_i32 s3, s3, 31
	s_sub_i32 s2, s2, s24
	s_mul_i32 s3, s3, s4
	v_mad_u64_u32 v[0:1], s[24:25], v0, s4, 0
	s_lshl_b32 s2, s2, 7
	v_add_u32_e32 v1, s3, v1
	s_waitcnt lgkmcnt(0)
	v_lshl_add_u64 v[0:1], v[0:1], 2, s[0:1]
	s_ashr_i32 s3, s2, 31
	v_lshl_add_u64 v[0:1], s[2:3], 2, v[0:1]
	v_lshl_add_u64 v[0:1], v[0:1], 0, v[142:143]
	s_lshl_b64 s[0:1], s[4:5], 5
	v_lshl_add_u64 v[2:3], v[0:1], 0, s[0:1]
	v_lshl_add_u64 v[4:5], v[2:3], 0, s[0:1]
	global_load_dwordx4 v[120:123], v[2:3], off nt
	global_load_dwordx4 v[116:119], v[4:5], off nt
	v_lshl_add_u64 v[2:3], v[4:5], 0, s[0:1]
	v_lshl_add_u64 v[4:5], v[2:3], 0, s[0:1]
	global_load_dwordx4 v[108:111], v[2:3], off nt
	global_load_dwordx4 v[100:103], v[4:5], off nt
	v_lshl_add_u64 v[2:3], v[4:5], 0, s[0:1]
	v_lshl_add_u64 v[4:5], v[2:3], 0, s[0:1]
	v_lshl_add_u64 v[6:7], v[4:5], 0, s[0:1]
	v_mad_u64_u32 v[8:9], s[2:3], s4, v164, v[6:7]
	v_subrev_u32_e32 v9, s4, v9
	v_lshl_add_u64 v[10:11], v[8:9], 0, s[0:1]
	v_lshl_add_u64 v[12:13], v[10:11], 0, s[0:1]
	v_lshl_add_u64 v[14:15], v[12:13], 0, s[0:1]
	v_lshl_add_u64 v[16:17], v[14:15], 0, s[0:1]
	v_lshl_add_u64 v[18:19], v[16:17], 0, s[0:1]
	v_lshl_add_u64 v[20:21], v[18:19], 0, s[0:1]
	v_mad_u64_u32 v[22:23], s[2:3], s4, v164, v[20:21]
	v_subrev_u32_e32 v23, s4, v23
	v_lshl_add_u64 v[24:25], v[22:23], 0, s[0:1]
	v_lshl_add_u64 v[26:27], v[24:25], 0, s[0:1]
	v_lshl_add_u64 v[28:29], v[26:27], 0, s[0:1]
	v_lshl_add_u64 v[30:31], v[28:29], 0, s[0:1]
	v_lshl_add_u64 v[32:33], v[30:31], 0, s[0:1]
	v_lshl_add_u64 v[34:35], v[32:33], 0, s[0:1]
	v_mad_u64_u32 v[128:129], s[2:3], s4, v164, v[34:35]
	global_load_dwordx4 v[112:115], v[2:3], off nt
	global_load_dwordx4 v[104:107], v[4:5], off nt
	global_load_dwordx4 v[96:99], v[6:7], off nt
	global_load_dwordx4 v[88:91], v[8:9], off offset:128 nt
	global_load_dwordx4 v[84:87], v[10:11], off offset:128 nt
	global_load_dwordx4 v[80:83], v[12:13], off offset:128 nt
	global_load_dwordx4 v[76:79], v[14:15], off offset:128 nt
	global_load_dwordx4 v[72:75], v[16:17], off offset:128 nt
	global_load_dwordx4 v[68:71], v[18:19], off offset:128 nt
	global_load_dwordx4 v[64:67], v[20:21], off offset:128 nt
	global_load_dwordx4 v[56:59], v[22:23], off offset:256 nt
	global_load_dwordx4 v[52:55], v[24:25], off offset:256 nt
	global_load_dwordx4 v[48:51], v[26:27], off offset:256 nt
	global_load_dwordx4 v[44:47], v[28:29], off offset:256 nt
	global_load_dwordx4 v[40:43], v[30:31], off offset:256 nt
	global_load_dwordx4 v[36:39], v[32:33], off offset:256 nt
	s_nop 0
	global_load_dwordx4 v[32:35], v[34:35], off offset:256 nt
	s_nop 0
	global_load_dwordx4 v[124:127], v[0:1], off nt
	global_load_dwordx4 v[92:95], v[0:1], off offset:128 nt
	global_load_dwordx4 v[60:63], v[0:1], off offset:256 nt
	global_load_dwordx4 v[28:31], v[0:1], off offset:384 nt
	v_subrev_u32_e32 v129, s4, v129
	v_lshl_add_u64 v[0:1], v[128:129], 0, s[0:1]
	v_lshl_add_u64 v[2:3], v[0:1], 0, s[0:1]
	global_load_dwordx4 v[20:23], v[0:1], off offset:384 nt
	v_lshl_add_u64 v[0:1], v[2:3], 0, s[0:1]
	global_load_dwordx4 v[16:19], v[2:3], off offset:384 nt
	v_lshl_add_u64 v[2:3], v[0:1], 0, s[0:1]
	global_load_dwordx4 v[12:15], v[0:1], off offset:384 nt
	v_lshl_add_u64 v[0:1], v[2:3], 0, s[0:1]
	global_load_dwordx4 v[8:11], v[2:3], off offset:384 nt
	v_lshl_add_u64 v[2:3], v[0:1], 0, s[0:1]
	global_load_dwordx4 v[24:27], v[128:129], off offset:384 nt
	global_load_dwordx4 v[4:7], v[0:1], off offset:384 nt
	s_nop 0
	global_load_dwordx4 v[0:3], v[2:3], off offset:384 nt
	s_lshr_b32 s4, s4, 5
	v_cvt_f32_u32_e32 v128, s4
	s_sub_i32 s3, 0, s4
	s_abs_i32 s2, s58
	s_mov_b64 s[0:1], -1
	v_rcp_iflag_f32_e32 v128, v128
	s_nop 0
	v_mul_f32_e32 v128, 0x4f7ffffe, v128
	v_cvt_u32_f32_e32 v128, v128
	s_nop 0
	v_readfirstlane_b32 s56, v128
	s_mul_i32 s3, s3, s56
	s_mul_hi_u32 s3, s56, s3
	s_add_i32 s56, s56, s3
	s_mul_hi_u32 s3, s2, s56
	s_mul_i32 s24, s3, s4
	s_sub_i32 s60, s2, s24
	s_add_i32 s2, s3, 1
	s_sub_i32 s61, s60, s4
	s_cmp_ge_u32 s60, s4
	s_cselect_b32 s2, s2, s3
	s_cselect_b32 s3, s61, s60
	s_add_i32 s24, s2, 1
	s_cmp_ge_u32 s3, s4
	s_cselect_b32 s2, s24, s2
	s_xor_b32 s2, s2, s59
	s_sub_i32 s38, s2, s59
	s_lshl_b32 s36, s38, 6
	s_cmp_lg_u64 s[22:23], 0
	s_cselect_b64 s[24:25], -1, 0
	s_cmp_eq_u64 s[22:23], 0
	s_cbranch_scc1 .Lgain_skip
	v_or_b32_e32 v196, s36, v136
	v_ashrrev_i32_e32 v197, 31, v196
	v_lshl_add_u64 v[196:197], v[196:197], 2, s[22:23]
	global_load_dword v198, v[196:197], off
	global_load_dword v199, v[196:197], off offset:32
	global_load_dword v200, v[196:197], off offset:64
	global_load_dword v201, v[196:197], off offset:96
	global_load_dword v202, v[196:197], off offset:128
	global_load_dword v203, v[196:197], off offset:160
	global_load_dword v204, v[196:197], off offset:192
	global_load_dword v205, v[196:197], off offset:224
	s_waitcnt vmcnt(0)
.Lgain_skip:
	s_and_b64 vcc, exec, s[34:35]
	s_cbranch_vccz .LBB0_125
	s_cmp_lt_i32 s57, 1
	s_cbranch_scc1 .LBB0_110
	s_cmp_lt_i32 s57, 2
	s_cbranch_scc1 .LBB0_95
	s_cmp_lg_u32 s57, 2
	s_cbranch_scc0 .LBB0_81
	v_cndmask_b32_e64 v128, 0, 1, s[24:25]
	v_cmp_ne_u32_e64 s[2:3], 1, v128
	s_andn2_b64 vcc, exec, s[24:25]
	s_cbranch_vccnz .LBB0_854
	v_or_b32_e32 v128, s36, v136
	s_ashr_i32 s37, s36, 31
	v_ashrrev_i32_e32 v129, 31, v128
	v_lshl_add_u64 v[130:131], s[36:37], 0, v[136:137]
	v_lshl_add_u64 v[128:129], v[128:129], 2, s[22:23]
	v_lshl_add_u64 v[130:131], v[130:131], 2, s[22:23]
	v_mov_b32_e32 v128, v198
	s_nop 0
	v_mov_b32_e32 v132, v199
	v_pk_mul_f32 v[134:135], v[126:127], v[128:129] op_sel_hi:[1,0]
	v_pk_mul_f32 v[168:169], v[124:125], v[128:129] op_sel_hi:[1,0]
	v_pk_mul_f32 v[130:131], v[122:123], v[132:133] op_sel_hi:[1,0]
	v_pk_mul_f32 v[128:129], v[120:121], v[132:133] op_sel_hi:[1,0]
	ds_write2_b32 v145, v168, v169 offset1:1
	ds_write2_b32 v145, v134, v135 offset0:2 offset1:3
	s_cbranch_execnz .LBB0_71

.LBB0_71:
	v_add_u32_e32 v132, v144, v147
	s_and_b64 vcc, exec, s[2:3]
	ds_write2_b32 v132, v128, v129 offset1:1
	ds_write2_b32 v132, v130, v131 offset0:2 offset1:3
	s_cbranch_vccnz .LBB0_855
	s_ashr_i32 s37, s36, 31
	v_lshl_add_u64 v[128:129], s[36:37], 0, v[136:137]
	v_lshl_add_u64 v[128:129], v[128:129], 2, s[22:23]
	v_mov_b32_e32 v130, v200
	s_nop 0
	v_mov_b32_e32 v128, v201
	v_pk_mul_f32 v[132:133], v[118:119], v[130:131] op_sel_hi:[1,0]
	v_pk_mul_f32 v[134:135], v[116:117], v[130:131] op_sel_hi:[1,0]
	v_pk_mul_f32 v[130:131], v[110:111], v[128:129] op_sel_hi:[1,0]
	v_pk_mul_f32 v[128:129], v[108:109], v[128:129] op_sel_hi:[1,0]
	ds_write2_b32 v149, v134, v135 offset1:1
	ds_write2_b32 v149, v132, v133 offset0:2 offset1:3
	s_cbranch_execnz .LBB0_74

.LBB0_74:
	v_add_u32_e32 v132, v144, v151
	s_and_b64 vcc, exec, s[2:3]
	ds_write2_b32 v132, v128, v129 offset1:1
	ds_write2_b32 v132, v130, v131 offset0:2 offset1:3
	s_cbranch_vccnz .LBB0_856
	s_ashr_i32 s37, s36, 31
	v_lshl_add_u64 v[128:129], s[36:37], 0, v[136:137]
	v_lshl_add_u64 v[128:129], v[128:129], 2, s[22:23]
	v_mov_b32_e32 v130, v202
	s_nop 0
	v_mov_b32_e32 v128, v203
	v_pk_mul_f32 v[132:133], v[102:103], v[130:131] op_sel_hi:[1,0]
	v_pk_mul_f32 v[134:135], v[100:101], v[130:131] op_sel_hi:[1,0]
	v_pk_mul_f32 v[130:131], v[114:115], v[128:129] op_sel_hi:[1,0]
	v_pk_mul_f32 v[128:129], v[112:113], v[128:129] op_sel_hi:[1,0]
	ds_write2_b32 v152, v134, v135 offset1:1
	ds_write2_b32 v152, v132, v133 offset0:2 offset1:3
	s_cbranch_execnz .LBB0_77

.LBB0_77:
	v_add_u32_e32 v132, v144, v153
	s_and_b64 vcc, exec, s[2:3]
	ds_write2_b32 v132, v128, v129 offset1:1
	ds_write2_b32 v132, v130, v131 offset0:2 offset1:3
	s_cbranch_vccnz .LBB0_857
	s_ashr_i32 s37, s36, 31
	v_lshl_add_u64 v[128:129], s[36:37], 0, v[136:137]
	v_lshl_add_u64 v[128:129], v[128:129], 2, s[22:23]
	v_mov_b32_e32 v130, v204
	s_nop 0
	v_mov_b32_e32 v128, v205
	v_pk_mul_f32 v[132:133], v[106:107], v[130:131] op_sel_hi:[1,0]
	v_pk_mul_f32 v[134:135], v[104:105], v[130:131] op_sel_hi:[1,0]
	v_pk_mul_f32 v[130:131], v[98:99], v[128:129] op_sel_hi:[1,0]
	v_pk_mul_f32 v[128:129], v[96:97], v[128:129] op_sel_hi:[1,0]
	ds_write2_b32 v154, v134, v135 offset1:1
	ds_write2_b32 v154, v132, v133 offset0:2 offset1:3
	s_cbranch_execnz .LBB0_80

.LBB0_81:
	s_and_b64 vcc, exec, s[0:1]
	s_cbranch_vccz .LBB0_821
	v_cndmask_b32_e64 v128, 0, 1, s[24:25]
	v_cmp_ne_u32_e64 s[2:3], 1, v128
	s_andn2_b64 vcc, exec, s[24:25]
	s_cbranch_vccnz .LBB0_858
	v_or_b32_e32 v128, s36, v136
	s_ashr_i32 s37, s36, 31
	v_ashrrev_i32_e32 v129, 31, v128
	v_lshl_add_u64 v[130:131], s[36:37], 0, v[136:137]
	v_lshl_add_u64 v[128:129], v[128:129], 2, s[22:23]
	v_lshl_add_u64 v[130:131], v[130:131], 2, s[22:23]
	v_mov_b32_e32 v128, v198
	s_nop 0
	v_mov_b32_e32 v132, v199
	v_pk_mul_f32 v[134:135], v[126:127], v[128:129] op_sel_hi:[1,0]
	v_pk_mul_f32 v[168:169], v[124:125], v[128:129] op_sel_hi:[1,0]
	v_pk_mul_f32 v[130:131], v[122:123], v[132:133] op_sel_hi:[1,0]
	v_pk_mul_f32 v[128:129], v[120:121], v[132:133] op_sel_hi:[1,0]
	ds_write2_b32 v145, v168, v169 offset1:1
	ds_write2_b32 v145, v134, v135 offset0:2 offset1:3
	s_cbranch_execnz .LBB0_85

.LBB0_96:
	v_cndmask_b32_e64 v128, 0, 1, s[24:25]
	v_cmp_ne_u32_e64 s[2:3], 1, v128
	s_andn2_b64 vcc, exec, s[24:25]
	s_cbranch_vccnz .LBB0_825
	v_or_b32_e32 v128, s36, v136
	s_ashr_i32 s37, s36, 31
	v_ashrrev_i32_e32 v129, 31, v128
	v_lshl_add_u64 v[130:131], s[36:37], 0, v[136:137]
	v_lshl_add_u64 v[128:129], v[128:129], 2, s[22:23]
	v_lshl_add_u64 v[130:131], v[130:131], 2, s[22:23]
	v_mov_b32_e32 v128, v198
	s_nop 0
	v_mov_b32_e32 v132, v199
	v_pk_mul_f32 v[134:135], v[126:127], v[128:129] op_sel_hi:[1,0]
	v_pk_mul_f32 v[168:169], v[124:125], v[128:129] op_sel_hi:[1,0]
	v_pk_mul_f32 v[130:131], v[122:123], v[132:133] op_sel_hi:[1,0]
	v_pk_mul_f32 v[128:129], v[120:121], v[132:133] op_sel_hi:[1,0]
	ds_write2_b32 v145, v168, v169 offset1:1
	ds_write2_b32 v145, v134, v135 offset0:2 offset1:3
	s_cbranch_execnz .LBB0_99

.LBB0_110:
	s_andn2_b64 vcc, exec, s[0:1]
	s_cbranch_vccnz .LBB0_124
	v_cndmask_b32_e64 v128, 0, 1, s[24:25]
	v_cmp_ne_u32_e64 s[2:3], 1, v128
	s_andn2_b64 vcc, exec, s[24:25]
	s_cbranch_vccnz .LBB0_803
	v_or_b32_e32 v128, s36, v136
	s_ashr_i32 s37, s36, 31
	v_ashrrev_i32_e32 v129, 31, v128
	v_lshl_add_u64 v[130:131], s[36:37], 0, v[136:137]
	v_lshl_add_u64 v[128:129], v[128:129], 2, s[22:23]
	v_lshl_add_u64 v[130:131], v[130:131], 2, s[22:23]
	v_mov_b32_e32 v128, v198
	s_nop 0
	v_mov_b32_e32 v132, v199
	v_pk_mul_f32 v[134:135], v[126:127], v[128:129] op_sel_hi:[1,0]
	v_pk_mul_f32 v[168:169], v[124:125], v[128:129] op_sel_hi:[1,0]
	v_pk_mul_f32 v[130:131], v[122:123], v[132:133] op_sel_hi:[1,0]
	v_pk_mul_f32 v[128:129], v[120:121], v[132:133] op_sel_hi:[1,0]
	ds_write2_b32 v145, v168, v169 offset1:1
	ds_write2_b32 v145, v134, v135 offset0:2 offset1:3
	s_cbranch_execnz .LBB0_114

.LBB0_125:
	s_and_b64 vcc, exec, s[0:1]
	s_cbranch_vccz .LBB0_250
	s_waitcnt vmcnt(10)
	v_pk_mul_f32 v[126:127], v[126:127], s[16:17] op_sel_hi:[1,0]
	v_pk_mul_f32 v[124:125], v[124:125], s[16:17] op_sel_hi:[1,0]
	s_cmp_lt_i32 s57, 4
	s_mov_b64 s[0:1], -1
	s_cbranch_scc1 .LBB0_187
	s_cmp_lt_i32 s57, 5
	s_cbranch_scc1 .LBB0_167
	s_cmp_gt_i32 s57, 5
	s_cbranch_scc0 .LBB0_147
	v_cndmask_b32_e64 v128, 0, 1, s[24:25]
	v_cmp_ne_u32_e64 s[2:3], 1, v128
	v_mov_b64_e32 v[130:131], v[126:127]
	s_andn2_b64 vcc, exec, s[24:25]
	v_mov_b64_e32 v[128:129], v[124:125]
	s_cbranch_vccnz .LBB0_131
	v_or_b32_e32 v128, s36, v136
	v_ashrrev_i32_e32 v129, 31, v128
	v_lshl_add_u64 v[128:129], v[128:129], 2, s[22:23]
	v_mov_b32_e32 v128, v198
	v_pk_mul_f32 v[130:131], v[126:127], v[128:129] op_sel_hi:[1,0]
	v_pk_mul_f32 v[128:129], v[124:125], v[128:129] op_sel_hi:[1,0]
.LBB0_131:
	ds_write2_b32 v145, v128, v129 offset1:1
	ds_write2_b32 v145, v130, v131 offset0:2 offset1:3
	v_pk_mul_f32 v[128:129], v[122:123], s[16:17] op_sel_hi:[1,0]
	s_and_b64 vcc, exec, s[2:3]
	v_pk_mul_f32 v[130:131], v[120:121], s[16:17] op_sel_hi:[1,0]
	s_cbranch_vccnz .LBB0_133
	s_ashr_i32 s37, s36, 31
	v_lshl_add_u64 v[132:133], s[36:37], 0, v[136:137]
	v_lshl_add_u64 v[132:133], v[132:133], 2, s[22:23]
	v_mov_b32_e32 v132, v199
	v_pk_mul_f32 v[128:129], v[128:129], v[132:133] op_sel_hi:[1,0]
	v_pk_mul_f32 v[130:131], v[130:131], v[132:133] op_sel_hi:[1,0]
.LBB0_133:
	v_add_u32_e32 v132, v144, v147
	ds_write2_b32 v132, v130, v131 offset1:1
	ds_write2_b32 v132, v128, v129 offset0:2 offset1:3
	v_pk_mul_f32 v[128:129], v[118:119], s[16:17] op_sel_hi:[1,0]
	s_and_b64 vcc, exec, s[2:3]
	v_pk_mul_f32 v[130:131], v[116:117], s[16:17] op_sel_hi:[1,0]
	s_cbranch_vccnz .LBB0_135
	s_ashr_i32 s37, s36, 31
	v_lshl_add_u64 v[132:133], s[36:37], 0, v[136:137]
	v_lshl_add_u64 v[132:133], v[132:133], 2, s[22:23]
	v_mov_b32_e32 v132, v200
	v_pk_mul_f32 v[128:129], v[128:129], v[132:133] op_sel_hi:[1,0]
	v_pk_mul_f32 v[130:131], v[130:131], v[132:133] op_sel_hi:[1,0]
.LBB0_135:
	ds_write2_b32 v149, v130, v131 offset1:1
	ds_write2_b32 v149, v128, v129 offset0:2 offset1:3
	v_pk_mul_f32 v[128:129], v[110:111], s[16:17] op_sel_hi:[1,0]
	s_and_b64 vcc, exec, s[2:3]
	v_pk_mul_f32 v[130:131], v[108:109], s[16:17] op_sel_hi:[1,0]
	s_cbranch_vccnz .LBB0_137
	s_ashr_i32 s37, s36, 31
	v_lshl_add_u64 v[132:133], s[36:37], 0, v[136:137]
	v_lshl_add_u64 v[132:133], v[132:133], 2, s[22:23]
	v_mov_b32_e32 v132, v201
	v_pk_mul_f32 v[128:129], v[128:129], v[132:133] op_sel_hi:[1,0]
	v_pk_mul_f32 v[130:131], v[130:131], v[132:133] op_sel_hi:[1,0]
.LBB0_137:
	v_add_u32_e32 v132, v144, v151
	ds_write2_b32 v132, v130, v131 offset1:1
	ds_write2_b32 v132, v128, v129 offset0:2 offset1:3
	v_pk_mul_f32 v[128:129], v[102:103], s[16:17] op_sel_hi:[1,0]
	s_and_b64 vcc, exec, s[2:3]
	v_pk_mul_f32 v[130:131], v[100:101], s[16:17] op_sel_hi:[1,0]
	s_cbranch_vccnz .LBB0_139
	s_ashr_i32 s37, s36, 31
	v_lshl_add_u64 v[132:133], s[36:37], 0, v[136:137]
	v_lshl_add_u64 v[132:133], v[132:133], 2, s[22:23]
	v_mov_b32_e32 v132, v202
	v_pk_mul_f32 v[128:129], v[128:129], v[132:133] op_sel_hi:[1,0]
	v_pk_mul_f32 v[130:131], v[130:131], v[132:133] op_sel_hi:[1,0]
.LBB0_139:
	ds_write2_b32 v152, v130, v131 offset1:1
	ds_write2_b32 v152, v128, v129 offset0:2 offset1:3
	v_pk_mul_f32 v[128:129], v[114:115], s[16:17] op_sel_hi:[1,0]
	s_and_b64 vcc, exec, s[2:3]
	v_pk_mul_f32 v[130:131], v[112:113], s[16:17] op_sel_hi:[1,0]
	s_cbranch_vccnz .LBB0_141
	s_ashr_i32 s37, s36, 31
	v_lshl_add_u64 v[132:133], s[36:37], 0, v[136:137]
	v_lshl_add_u64 v[132:133], v[132:133], 2, s[22:23]
	v_mov_b32_e32 v132, v203
	v_pk_mul_f32 v[128:129], v[128:129], v[132:133] op_sel_hi:[1,0]
	v_pk_mul_f32 v[130:131], v[130:131], v[132:133] op_sel_hi:[1,0]
.LBB0_141:
	v_add_u32_e32 v132, v144, v153
	ds_write2_b32 v132, v130, v131 offset1:1
	ds_write2_b32 v132, v128, v129 offset0:2 offset1:3
	v_pk_mul_f32 v[128:129], v[106:107], s[16:17] op_sel_hi:[1,0]
	s_and_b64 vcc, exec, s[2:3]
	v_pk_mul_f32 v[130:131], v[104:105], s[16:17] op_sel_hi:[1,0]
	s_cbranch_vccnz .LBB0_143
	s_ashr_i32 s37, s36, 31
	v_lshl_add_u64 v[132:133], s[36:37], 0, v[136:137]
	v_lshl_add_u64 v[132:133], v[132:133], 2, s[22:23]
	v_mov_b32_e32 v132, v204
	v_pk_mul_f32 v[128:129], v[128:129], v[132:133] op_sel_hi:[1,0]
	v_pk_mul_f32 v[130:131], v[130:131], v[132:133] op_sel_hi:[1,0]
.LBB0_143:
	ds_write2_b32 v154, v130, v131 offset1:1
	ds_write2_b32 v154, v128, v129 offset0:2 offset1:3
	v_pk_mul_f32 v[130:131], v[98:99], s[16:17] op_sel_hi:[1,0]
	v_pk_mul_f32 v[128:129], v[96:97], s[16:17] op_sel_hi:[1,0]
	s_and_b64 vcc, exec, s[24:25]
	s_cbranch_vccz .LBB0_862
	s_ashr_i32 s37, s36, 31
	v_lshl_add_u64 v[132:133], s[36:37], 0, v[136:137]
	v_lshl_add_u64 v[132:133], v[132:133], 2, s[22:23]
	v_mov_b32_e32 v132, v205
	v_pk_mul_f32 v[134:135], v[130:131], v[132:133] op_sel_hi:[1,0]
	v_pk_mul_f32 v[132:133], v[128:129], v[132:133] op_sel_hi:[1,0]
	s_cbranch_execnz .LBB0_146

.LBB0_147:
	s_and_b64 vcc, exec, s[0:1]
	s_cbranch_vccz .LBB0_166
	v_cndmask_b32_e64 v128, 0, 1, s[24:25]
	v_cmp_ne_u32_e64 s[2:3], 1, v128
	v_mov_b64_e32 v[130:131], v[126:127]
	s_andn2_b64 vcc, exec, s[24:25]
	v_mov_b64_e32 v[128:129], v[124:125]
	s_cbranch_vccnz .LBB0_150
	v_or_b32_e32 v128, s36, v136
	v_ashrrev_i32_e32 v129, 31, v128
	v_lshl_add_u64 v[128:129], v[128:129], 2, s[22:23]
	v_mov_b32_e32 v128, v198
	v_pk_mul_f32 v[130:131], v[126:127], v[128:129] op_sel_hi:[1,0]
	v_pk_mul_f32 v[128:129], v[124:125], v[128:129] op_sel_hi:[1,0]

.LBB0_167:
	s_andn2_b64 vcc, exec, s[0:1]
	s_cbranch_vccnz .LBB0_186
	v_cndmask_b32_e64 v128, 0, 1, s[24:25]
	v_cmp_ne_u32_e64 s[2:3], 1, v128
	v_mov_b64_e32 v[130:131], v[126:127]
	s_andn2_b64 vcc, exec, s[24:25]
	v_mov_b64_e32 v[128:129], v[124:125]
	s_cbranch_vccnz .LBB0_170
	v_or_b32_e32 v128, s36, v136
	v_ashrrev_i32_e32 v129, 31, v128
	v_lshl_add_u64 v[128:129], v[128:129], 2, s[22:23]
	v_mov_b32_e32 v128, v198
	v_pk_mul_f32 v[130:131], v[126:127], v[128:129] op_sel_hi:[1,0]
	v_pk_mul_f32 v[128:129], v[124:125], v[128:129] op_sel_hi:[1,0]

.LBB0_193:
	s_cmp_eq_u32 s57, 2
	s_mov_b64 s[2:3], -1
	s_cbranch_scc0 .LBB0_212
	v_cndmask_b32_e64 v128, 0, 1, s[24:25]
	v_cmp_ne_u32_e64 s[2:3], 1, v128
	v_mov_b64_e32 v[130:131], v[126:127]
	s_andn2_b64 vcc, exec, s[24:25]
	v_mov_b64_e32 v[128:129], v[124:125]
	s_cbranch_vccnz .LBB0_196
	v_or_b32_e32 v128, s36, v136
	v_ashrrev_i32_e32 v129, 31, v128
	v_lshl_add_u64 v[128:129], v[128:129], 2, s[22:23]
	v_mov_b32_e32 v128, v198
	v_pk_mul_f32 v[130:131], v[126:127], v[128:129] op_sel_hi:[1,0]
	v_pk_mul_f32 v[128:129], v[124:125], v[128:129] op_sel_hi:[1,0]

.LBB0_214:
	v_cndmask_b32_e64 v128, 0, 1, s[24:25]
	v_cmp_ne_u32_e64 s[2:3], 1, v128
	v_mov_b64_e32 v[130:131], v[126:127]
	s_andn2_b64 vcc, exec, s[24:25]
	v_mov_b64_e32 v[128:129], v[124:125]
	s_cbranch_vccnz .LBB0_216
	v_or_b32_e32 v128, s36, v136
	v_ashrrev_i32_e32 v129, 31, v128
	v_lshl_add_u64 v[128:129], v[128:129], 2, s[22:23]
	v_mov_b32_e32 v128, v198
	v_pk_mul_f32 v[130:131], v[126:127], v[128:129] op_sel_hi:[1,0]
	v_pk_mul_f32 v[128:129], v[124:125], v[128:129] op_sel_hi:[1,0]

.LBB0_232:
	v_cndmask_b32_e64 v128, 0, 1, s[24:25]
	v_cmp_ne_u32_e64 s[2:3], 1, v128
	s_andn2_b64 vcc, exec, s[24:25]
	s_cbranch_vccnz .LBB0_234
	v_or_b32_e32 v128, s36, v136
	v_ashrrev_i32_e32 v129, 31, v128
	v_lshl_add_u64 v[128:129], v[128:129], 2, s[22:23]
	v_mov_b32_e32 v128, v198
	v_pk_mul_f32 v[126:127], v[126:127], v[128:129] op_sel_hi:[1,0]
	v_pk_mul_f32 v[124:125], v[124:125], v[128:129] op_sel_hi:[1,0]
.LBB0_234:
	v_pk_mul_f32 v[122:123], v[122:123], s[16:17] op_sel_hi:[1,0]
	s_and_b64 vcc, exec, s[2:3]
	v_pk_mul_f32 v[120:121], v[120:121], s[16:17] op_sel_hi:[1,0]
	ds_write2_b32 v145, v124, v125 offset1:1
	ds_write2_b32 v145, v126, v127 offset0:2 offset1:3
	s_cbranch_vccnz .LBB0_236
	s_ashr_i32 s37, s36, 31
	v_lshl_add_u64 v[124:125], s[36:37], 0, v[136:137]
	v_lshl_add_u64 v[124:125], v[124:125], 2, s[22:23]
	v_mov_b32_e32 v124, v199
	v_pk_mul_f32 v[122:123], v[122:123], v[124:125] op_sel_hi:[1,0]
	v_pk_mul_f32 v[120:121], v[120:121], v[124:125] op_sel_hi:[1,0]
.LBB0_236:
	v_add_u32_e32 v124, v144, v147
	v_pk_mul_f32 v[118:119], v[118:119], s[16:17] op_sel_hi:[1,0]
	s_and_b64 vcc, exec, s[2:3]
	v_pk_mul_f32 v[116:117], v[116:117], s[16:17] op_sel_hi:[1,0]
	ds_write2_b32 v124, v120, v121 offset1:1
	ds_write2_b32 v124, v122, v123 offset0:2 offset1:3
	s_cbranch_vccnz .LBB0_238
	s_ashr_i32 s37, s36, 31
	v_lshl_add_u64 v[120:121], s[36:37], 0, v[136:137]
	v_lshl_add_u64 v[120:121], v[120:121], 2, s[22:23]
	v_mov_b32_e32 v120, v200
	v_pk_mul_f32 v[118:119], v[118:119], v[120:121] op_sel_hi:[1,0]
	v_pk_mul_f32 v[116:117], v[116:117], v[120:121] op_sel_hi:[1,0]
.LBB0_238:
	v_pk_mul_f32 v[110:111], v[110:111], s[16:17] op_sel_hi:[1,0]
	s_and_b64 vcc, exec, s[2:3]
	v_pk_mul_f32 v[108:109], v[108:109], s[16:17] op_sel_hi:[1,0]
	ds_write2_b32 v149, v116, v117 offset1:1
	ds_write2_b32 v149, v118, v119 offset0:2 offset1:3
	s_cbranch_vccnz .LBB0_240
	s_ashr_i32 s37, s36, 31
	v_lshl_add_u64 v[116:117], s[36:37], 0, v[136:137]
	v_lshl_add_u64 v[116:117], v[116:117], 2, s[22:23]
	v_mov_b32_e32 v116, v201
	v_pk_mul_f32 v[110:111], v[110:111], v[116:117] op_sel_hi:[1,0]
	v_pk_mul_f32 v[108:109], v[108:109], v[116:117] op_sel_hi:[1,0]
.LBB0_240:
	v_add_u32_e32 v116, v144, v151
	v_pk_mul_f32 v[102:103], v[102:103], s[16:17] op_sel_hi:[1,0]
	s_and_b64 vcc, exec, s[2:3]
	v_pk_mul_f32 v[100:101], v[100:101], s[16:17] op_sel_hi:[1,0]
	ds_write2_b32 v116, v108, v109 offset1:1
	ds_write2_b32 v116, v110, v111 offset0:2 offset1:3
	s_cbranch_vccnz .LBB0_242
	s_ashr_i32 s37, s36, 31
	v_lshl_add_u64 v[108:109], s[36:37], 0, v[136:137]
	v_lshl_add_u64 v[108:109], v[108:109], 2, s[22:23]
	v_mov_b32_e32 v108, v202
	v_pk_mul_f32 v[102:103], v[102:103], v[108:109] op_sel_hi:[1,0]
	v_pk_mul_f32 v[100:101], v[100:101], v[108:109] op_sel_hi:[1,0]
.LBB0_242:
	ds_write2_b32 v152, v100, v101 offset1:1
	ds_write2_b32 v152, v102, v103 offset0:2 offset1:3
	v_pk_mul_f32 v[100:101], v[114:115], s[16:17] op_sel_hi:[1,0]
	s_and_b64 vcc, exec, s[2:3]
	v_pk_mul_f32 v[102:103], v[112:113], s[16:17] op_sel_hi:[1,0]
	s_cbranch_vccnz .LBB0_244
	s_ashr_i32 s37, s36, 31
	v_lshl_add_u64 v[108:109], s[36:37], 0, v[136:137]
	v_lshl_add_u64 v[108:109], v[108:109], 2, s[22:23]
	v_mov_b32_e32 v108, v203
	v_pk_mul_f32 v[100:101], v[100:101], v[108:109] op_sel_hi:[1,0]
	v_pk_mul_f32 v[102:103], v[102:103], v[108:109] op_sel_hi:[1,0]
.LBB0_244:
	v_add_u32_e32 v108, v144, v153
	ds_write2_b32 v108, v102, v103 offset1:1
	ds_write2_b32 v108, v100, v101 offset0:2 offset1:3
	v_pk_mul_f32 v[100:101], v[106:107], s[16:17] op_sel_hi:[1,0]
	s_and_b64 vcc, exec, s[2:3]
	v_pk_mul_f32 v[102:103], v[104:105], s[16:17] op_sel_hi:[1,0]
	s_cbranch_vccnz .LBB0_246
	s_ashr_i32 s37, s36, 31
	v_lshl_add_u64 v[104:105], s[36:37], 0, v[136:137]
	v_lshl_add_u64 v[104:105], v[104:105], 2, s[22:23]
	v_mov_b32_e32 v104, v204
	v_pk_mul_f32 v[100:101], v[100:101], v[104:105] op_sel_hi:[1,0]
	v_pk_mul_f32 v[102:103], v[102:103], v[104:105] op_sel_hi:[1,0]
.LBB0_246:
	v_pk_mul_f32 v[98:99], v[98:99], s[16:17] op_sel_hi:[1,0]
	v_pk_mul_f32 v[96:97], v[96:97], s[16:17] op_sel_hi:[1,0]
	s_and_b64 vcc, exec, s[24:25]
	ds_write2_b32 v154, v102, v103 offset1:1
	ds_write2_b32 v154, v100, v101 offset0:2 offset1:3
	s_cbranch_vccz .LBB0_831
	s_ashr_i32 s37, s36, 31
	v_lshl_add_u64 v[100:101], s[36:37], 0, v[136:137]
	v_lshl_add_u64 v[100:101], v[100:101], 2, s[22:23]
	v_mov_b32_e32 v100, v205
	v_pk_mul_f32 v[102:103], v[98:99], v[100:101] op_sel_hi:[1,0]
	v_pk_mul_f32 v[100:101], v[96:97], v[100:101] op_sel_hi:[1,0]
	s_cbranch_execnz .LBB0_249

.LBB0_250:
	s_add_i32 s60, s58, 1
	s_not_b32 s0, s58
	s_max_i32 s0, s60, s0
	s_mul_hi_u32 s1, s0, s56
	s_mul_i32 s2, s1, s4
	s_sub_i32 s0, s0, s2
	s_ashr_i32 s59, s60, 31
	s_add_i32 s2, s1, 1
	s_sub_i32 s3, s0, s4
	s_cmp_ge_u32 s0, s4
	s_cselect_b32 s1, s2, s1
	s_cselect_b32 s0, s3, s0
	s_add_i32 s2, s1, 1
	s_cmp_ge_u32 s0, s4
	s_cselect_b32 s0, s2, s1
	s_xor_b32 s0, s0, s59
	s_sub_i32 s38, s0, s59
	s_lshl_b32 s36, s38, 6
	s_mov_b64 s[0:1], -1
	s_and_b64 vcc, exec, s[34:35]
	s_cbranch_vccz .LBB0_311
	s_cmp_lt_i32 s57, 1
	s_cbranch_scc1 .LBB0_296
	s_cmp_lt_i32 s57, 2
	s_cbranch_scc1 .LBB0_281
	s_cmp_lg_u32 s57, 2
	s_cbranch_scc0 .LBB0_267
	s_waitcnt vmcnt(25)
	v_cndmask_b32_e64 v96, 0, 1, s[24:25]
	v_cmp_ne_u32_e64 s[2:3], 1, v96
	s_andn2_b64 vcc, exec, s[24:25]
	s_cbranch_vccnz .LBB0_865
	v_or_b32_e32 v96, s36, v136
	s_ashr_i32 s37, s36, 31
	v_ashrrev_i32_e32 v97, 31, v96
	v_lshl_add_u64 v[98:99], s[36:37], 0, v[136:137]
	v_lshl_add_u64 v[96:97], v[96:97], 2, s[22:23]
	v_lshl_add_u64 v[98:99], v[98:99], 2, s[22:23]
	v_mov_b32_e32 v96, v198
	s_nop 0
	v_mov_b32_e32 v100, v199
	v_pk_mul_f32 v[102:103], v[94:95], v[96:97] op_sel_hi:[1,0]
	v_pk_mul_f32 v[104:105], v[92:93], v[96:97] op_sel_hi:[1,0]
	v_pk_mul_f32 v[98:99], v[90:91], v[100:101] op_sel_hi:[1,0]
	v_pk_mul_f32 v[96:97], v[88:89], v[100:101] op_sel_hi:[1,0]
	ds_write2_b32 v145, v104, v105 offset1:1
	ds_write2_b32 v145, v102, v103 offset0:2 offset1:3
	s_cbranch_execnz .LBB0_257

.LBB0_257:
	v_add_u32_e32 v100, v144, v147
	s_and_b64 vcc, exec, s[2:3]
	ds_write2_b32 v100, v96, v97 offset1:1
	ds_write2_b32 v100, v98, v99 offset0:2 offset1:3
	s_cbranch_vccnz .LBB0_866
	s_ashr_i32 s37, s36, 31
	v_lshl_add_u64 v[96:97], s[36:37], 0, v[136:137]
	v_lshl_add_u64 v[96:97], v[96:97], 2, s[22:23]
	v_mov_b32_e32 v98, v200
	s_nop 0
	v_mov_b32_e32 v96, v201
	v_pk_mul_f32 v[100:101], v[86:87], v[98:99] op_sel_hi:[1,0]
	v_pk_mul_f32 v[102:103], v[84:85], v[98:99] op_sel_hi:[1,0]
	v_pk_mul_f32 v[98:99], v[82:83], v[96:97] op_sel_hi:[1,0]
	v_pk_mul_f32 v[96:97], v[80:81], v[96:97] op_sel_hi:[1,0]
	ds_write2_b32 v149, v102, v103 offset1:1
	ds_write2_b32 v149, v100, v101 offset0:2 offset1:3
	s_cbranch_execnz .LBB0_260

.LBB0_260:
	v_add_u32_e32 v100, v144, v151
	s_and_b64 vcc, exec, s[2:3]
	ds_write2_b32 v100, v96, v97 offset1:1
	ds_write2_b32 v100, v98, v99 offset0:2 offset1:3
	s_cbranch_vccnz .LBB0_867
	s_ashr_i32 s37, s36, 31
	v_lshl_add_u64 v[96:97], s[36:37], 0, v[136:137]
	v_lshl_add_u64 v[96:97], v[96:97], 2, s[22:23]
	v_mov_b32_e32 v98, v202
	s_nop 0
	v_mov_b32_e32 v96, v203
	v_pk_mul_f32 v[100:101], v[78:79], v[98:99] op_sel_hi:[1,0]
	v_pk_mul_f32 v[102:103], v[76:77], v[98:99] op_sel_hi:[1,0]
	v_pk_mul_f32 v[98:99], v[74:75], v[96:97] op_sel_hi:[1,0]
	v_pk_mul_f32 v[96:97], v[72:73], v[96:97] op_sel_hi:[1,0]
	ds_write2_b32 v152, v102, v103 offset1:1
	ds_write2_b32 v152, v100, v101 offset0:2 offset1:3
	s_cbranch_execnz .LBB0_263

.LBB0_263:
	v_add_u32_e32 v100, v144, v153
	s_and_b64 vcc, exec, s[2:3]
	ds_write2_b32 v100, v96, v97 offset1:1
	ds_write2_b32 v100, v98, v99 offset0:2 offset1:3
	s_cbranch_vccnz .LBB0_868
	s_ashr_i32 s37, s36, 31
	v_lshl_add_u64 v[96:97], s[36:37], 0, v[136:137]
	v_lshl_add_u64 v[96:97], v[96:97], 2, s[22:23]
	v_mov_b32_e32 v98, v204
	s_nop 0
	v_mov_b32_e32 v96, v205
	v_pk_mul_f32 v[100:101], v[70:71], v[98:99] op_sel_hi:[1,0]
	v_pk_mul_f32 v[102:103], v[68:69], v[98:99] op_sel_hi:[1,0]
	v_pk_mul_f32 v[98:99], v[66:67], v[96:97] op_sel_hi:[1,0]
	v_pk_mul_f32 v[96:97], v[64:65], v[96:97] op_sel_hi:[1,0]
	ds_write2_b32 v154, v102, v103 offset1:1
	ds_write2_b32 v154, v100, v101 offset0:2 offset1:3
	s_cbranch_execnz .LBB0_266

.LBB0_267:
	s_and_b64 vcc, exec, s[0:1]
	s_cbranch_vccz .LBB0_822
	s_waitcnt vmcnt(25)
	v_cndmask_b32_e64 v96, 0, 1, s[24:25]
	v_cmp_ne_u32_e64 s[2:3], 1, v96
	s_andn2_b64 vcc, exec, s[24:25]
	s_cbranch_vccnz .LBB0_869
	v_or_b32_e32 v96, s36, v136
	s_ashr_i32 s37, s36, 31
	v_ashrrev_i32_e32 v97, 31, v96
	v_lshl_add_u64 v[98:99], s[36:37], 0, v[136:137]
	v_lshl_add_u64 v[96:97], v[96:97], 2, s[22:23]
	v_lshl_add_u64 v[98:99], v[98:99], 2, s[22:23]
	v_mov_b32_e32 v96, v198
	s_nop 0
	v_mov_b32_e32 v100, v199
	v_pk_mul_f32 v[102:103], v[94:95], v[96:97] op_sel_hi:[1,0]
	v_pk_mul_f32 v[104:105], v[92:93], v[96:97] op_sel_hi:[1,0]
	v_pk_mul_f32 v[98:99], v[90:91], v[100:101] op_sel_hi:[1,0]
	v_pk_mul_f32 v[96:97], v[88:89], v[100:101] op_sel_hi:[1,0]
	ds_write2_b32 v145, v104, v105 offset1:1
	ds_write2_b32 v145, v102, v103 offset0:2 offset1:3
	s_cbranch_execnz .LBB0_271

.LBB0_282:
	s_waitcnt vmcnt(25)
	v_cndmask_b32_e64 v96, 0, 1, s[24:25]
	v_cmp_ne_u32_e64 s[2:3], 1, v96
	s_andn2_b64 vcc, exec, s[24:25]
	s_cbranch_vccnz .LBB0_832
	v_or_b32_e32 v96, s36, v136
	s_ashr_i32 s37, s36, 31
	v_ashrrev_i32_e32 v97, 31, v96
	v_lshl_add_u64 v[98:99], s[36:37], 0, v[136:137]
	v_lshl_add_u64 v[96:97], v[96:97], 2, s[22:23]
	v_lshl_add_u64 v[98:99], v[98:99], 2, s[22:23]
	v_mov_b32_e32 v96, v198
	s_nop 0
	v_mov_b32_e32 v100, v199
	v_pk_mul_f32 v[102:103], v[94:95], v[96:97] op_sel_hi:[1,0]
	v_pk_mul_f32 v[104:105], v[92:93], v[96:97] op_sel_hi:[1,0]
	v_pk_mul_f32 v[98:99], v[90:91], v[100:101] op_sel_hi:[1,0]
	v_pk_mul_f32 v[96:97], v[88:89], v[100:101] op_sel_hi:[1,0]
	ds_write2_b32 v145, v104, v105 offset1:1
	ds_write2_b32 v145, v102, v103 offset0:2 offset1:3
	s_cbranch_execnz .LBB0_285

.LBB0_296:
	s_andn2_b64 vcc, exec, s[0:1]
	s_cbranch_vccnz .LBB0_310
	s_waitcnt vmcnt(25)
	v_cndmask_b32_e64 v96, 0, 1, s[24:25]
	v_cmp_ne_u32_e64 s[2:3], 1, v96
	s_andn2_b64 vcc, exec, s[24:25]
	s_cbranch_vccnz .LBB0_807
	v_or_b32_e32 v96, s36, v136
	s_ashr_i32 s37, s36, 31
	v_ashrrev_i32_e32 v97, 31, v96
	v_lshl_add_u64 v[98:99], s[36:37], 0, v[136:137]
	v_lshl_add_u64 v[96:97], v[96:97], 2, s[22:23]
	v_lshl_add_u64 v[98:99], v[98:99], 2, s[22:23]
	v_mov_b32_e32 v96, v198
	s_nop 0
	v_mov_b32_e32 v100, v199
	v_pk_mul_f32 v[102:103], v[94:95], v[96:97] op_sel_hi:[1,0]
	v_pk_mul_f32 v[104:105], v[92:93], v[96:97] op_sel_hi:[1,0]
	v_pk_mul_f32 v[98:99], v[90:91], v[100:101] op_sel_hi:[1,0]
	v_pk_mul_f32 v[96:97], v[88:89], v[100:101] op_sel_hi:[1,0]
	ds_write2_b32 v145, v104, v105 offset1:1
	ds_write2_b32 v145, v102, v103 offset0:2 offset1:3
	s_cbranch_execnz .LBB0_300

.LBB0_311:
	s_and_b64 vcc, exec, s[0:1]
	s_cbranch_vccz .LBB0_435
	s_waitcnt vmcnt(9)
	v_pk_mul_f32 v[94:95], v[94:95], s[16:17] op_sel_hi:[1,0]
	v_pk_mul_f32 v[92:93], v[92:93], s[16:17] op_sel_hi:[1,0]
	s_cmp_lt_i32 s57, 4
	s_mov_b64 s[0:1], -1
	s_cbranch_scc1 .LBB0_373
	s_cmp_lt_i32 s57, 5
	s_cbranch_scc1 .LBB0_353
	s_cmp_gt_i32 s57, 5
	s_cbranch_scc0 .LBB0_333
	v_cndmask_b32_e64 v96, 0, 1, s[24:25]
	v_cmp_ne_u32_e64 s[2:3], 1, v96
	v_mov_b64_e32 v[98:99], v[94:95]
	s_andn2_b64 vcc, exec, s[24:25]
	v_mov_b64_e32 v[96:97], v[92:93]
	s_cbranch_vccnz .LBB0_317
	v_or_b32_e32 v96, s36, v136
	v_ashrrev_i32_e32 v97, 31, v96
	v_lshl_add_u64 v[96:97], v[96:97], 2, s[22:23]
	v_mov_b32_e32 v96, v198
	v_pk_mul_f32 v[98:99], v[94:95], v[96:97] op_sel_hi:[1,0]
	v_pk_mul_f32 v[96:97], v[92:93], v[96:97] op_sel_hi:[1,0]
.LBB0_317:
	ds_write2_b32 v145, v96, v97 offset1:1
	ds_write2_b32 v145, v98, v99 offset0:2 offset1:3
	v_pk_mul_f32 v[96:97], v[90:91], s[16:17] op_sel_hi:[1,0]
	s_and_b64 vcc, exec, s[2:3]
	v_pk_mul_f32 v[98:99], v[88:89], s[16:17] op_sel_hi:[1,0]
	s_cbranch_vccnz .LBB0_319
	s_ashr_i32 s37, s36, 31
	v_lshl_add_u64 v[100:101], s[36:37], 0, v[136:137]
	v_lshl_add_u64 v[100:101], v[100:101], 2, s[22:23]
	v_mov_b32_e32 v100, v199
	v_pk_mul_f32 v[96:97], v[96:97], v[100:101] op_sel_hi:[1,0]
	v_pk_mul_f32 v[98:99], v[98:99], v[100:101] op_sel_hi:[1,0]
.LBB0_319:
	v_add_u32_e32 v100, v144, v147
	ds_write2_b32 v100, v98, v99 offset1:1
	ds_write2_b32 v100, v96, v97 offset0:2 offset1:3
	v_pk_mul_f32 v[96:97], v[86:87], s[16:17] op_sel_hi:[1,0]
	s_and_b64 vcc, exec, s[2:3]
	v_pk_mul_f32 v[98:99], v[84:85], s[16:17] op_sel_hi:[1,0]
	s_cbranch_vccnz .LBB0_321
	s_ashr_i32 s37, s36, 31
	v_lshl_add_u64 v[100:101], s[36:37], 0, v[136:137]
	v_lshl_add_u64 v[100:101], v[100:101], 2, s[22:23]
	v_mov_b32_e32 v100, v200
	v_pk_mul_f32 v[96:97], v[96:97], v[100:101] op_sel_hi:[1,0]
	v_pk_mul_f32 v[98:99], v[98:99], v[100:101] op_sel_hi:[1,0]
.LBB0_321:
	ds_write2_b32 v149, v98, v99 offset1:1
	ds_write2_b32 v149, v96, v97 offset0:2 offset1:3
	v_pk_mul_f32 v[96:97], v[82:83], s[16:17] op_sel_hi:[1,0]
	s_and_b64 vcc, exec, s[2:3]
	v_pk_mul_f32 v[98:99], v[80:81], s[16:17] op_sel_hi:[1,0]
	s_cbranch_vccnz .LBB0_323
	s_ashr_i32 s37, s36, 31
	v_lshl_add_u64 v[100:101], s[36:37], 0, v[136:137]
	v_lshl_add_u64 v[100:101], v[100:101], 2, s[22:23]
	v_mov_b32_e32 v100, v201
	v_pk_mul_f32 v[96:97], v[96:97], v[100:101] op_sel_hi:[1,0]
	v_pk_mul_f32 v[98:99], v[98:99], v[100:101] op_sel_hi:[1,0]
.LBB0_323:
	v_add_u32_e32 v100, v144, v151
	ds_write2_b32 v100, v98, v99 offset1:1
	ds_write2_b32 v100, v96, v97 offset0:2 offset1:3
	v_pk_mul_f32 v[96:97], v[78:79], s[16:17] op_sel_hi:[1,0]
	s_and_b64 vcc, exec, s[2:3]
	v_pk_mul_f32 v[98:99], v[76:77], s[16:17] op_sel_hi:[1,0]
	s_cbranch_vccnz .LBB0_325
	s_ashr_i32 s37, s36, 31
	v_lshl_add_u64 v[100:101], s[36:37], 0, v[136:137]
	v_lshl_add_u64 v[100:101], v[100:101], 2, s[22:23]
	v_mov_b32_e32 v100, v202
	v_pk_mul_f32 v[96:97], v[96:97], v[100:101] op_sel_hi:[1,0]
	v_pk_mul_f32 v[98:99], v[98:99], v[100:101] op_sel_hi:[1,0]
.LBB0_325:
	ds_write2_b32 v152, v98, v99 offset1:1
	ds_write2_b32 v152, v96, v97 offset0:2 offset1:3
	v_pk_mul_f32 v[96:97], v[74:75], s[16:17] op_sel_hi:[1,0]
	s_and_b64 vcc, exec, s[2:3]
	v_pk_mul_f32 v[98:99], v[72:73], s[16:17] op_sel_hi:[1,0]
	s_cbranch_vccnz .LBB0_327
	s_ashr_i32 s37, s36, 31
	v_lshl_add_u64 v[100:101], s[36:37], 0, v[136:137]
	v_lshl_add_u64 v[100:101], v[100:101], 2, s[22:23]
	v_mov_b32_e32 v100, v203
	v_pk_mul_f32 v[96:97], v[96:97], v[100:101] op_sel_hi:[1,0]
	v_pk_mul_f32 v[98:99], v[98:99], v[100:101] op_sel_hi:[1,0]
.LBB0_327:
	v_add_u32_e32 v100, v144, v153
	ds_write2_b32 v100, v98, v99 offset1:1
	ds_write2_b32 v100, v96, v97 offset0:2 offset1:3
	v_pk_mul_f32 v[96:97], v[70:71], s[16:17] op_sel_hi:[1,0]
	s_and_b64 vcc, exec, s[2:3]
	v_pk_mul_f32 v[98:99], v[68:69], s[16:17] op_sel_hi:[1,0]
	s_cbranch_vccnz .LBB0_329
	s_ashr_i32 s37, s36, 31
	v_lshl_add_u64 v[100:101], s[36:37], 0, v[136:137]
	v_lshl_add_u64 v[100:101], v[100:101], 2, s[22:23]
	v_mov_b32_e32 v100, v204
	v_pk_mul_f32 v[96:97], v[96:97], v[100:101] op_sel_hi:[1,0]
	v_pk_mul_f32 v[98:99], v[98:99], v[100:101] op_sel_hi:[1,0]
.LBB0_329:
	ds_write2_b32 v154, v98, v99 offset1:1
	ds_write2_b32 v154, v96, v97 offset0:2 offset1:3
	v_pk_mul_f32 v[98:99], v[66:67], s[16:17] op_sel_hi:[1,0]
	v_pk_mul_f32 v[96:97], v[64:65], s[16:17] op_sel_hi:[1,0]
	s_and_b64 vcc, exec, s[24:25]
	s_cbranch_vccz .LBB0_873
	s_ashr_i32 s37, s36, 31
	v_lshl_add_u64 v[100:101], s[36:37], 0, v[136:137]
	v_lshl_add_u64 v[100:101], v[100:101], 2, s[22:23]
	v_mov_b32_e32 v100, v205
	v_pk_mul_f32 v[102:103], v[98:99], v[100:101] op_sel_hi:[1,0]
	v_pk_mul_f32 v[100:101], v[96:97], v[100:101] op_sel_hi:[1,0]
	s_cbranch_execnz .LBB0_332

.LBB0_333:
	s_and_b64 vcc, exec, s[0:1]
	s_cbranch_vccz .LBB0_352
	v_cndmask_b32_e64 v96, 0, 1, s[24:25]
	v_cmp_ne_u32_e64 s[2:3], 1, v96
	v_mov_b64_e32 v[98:99], v[94:95]
	s_andn2_b64 vcc, exec, s[24:25]
	v_mov_b64_e32 v[96:97], v[92:93]
	s_cbranch_vccnz .LBB0_336
	v_or_b32_e32 v96, s36, v136
	v_ashrrev_i32_e32 v97, 31, v96
	v_lshl_add_u64 v[96:97], v[96:97], 2, s[22:23]
	v_mov_b32_e32 v96, v198
	v_pk_mul_f32 v[98:99], v[94:95], v[96:97] op_sel_hi:[1,0]
	v_pk_mul_f32 v[96:97], v[92:93], v[96:97] op_sel_hi:[1,0]

.LBB0_353:
	s_andn2_b64 vcc, exec, s[0:1]
	s_cbranch_vccnz .LBB0_372
	v_cndmask_b32_e64 v96, 0, 1, s[24:25]
	v_cmp_ne_u32_e64 s[2:3], 1, v96
	v_mov_b64_e32 v[98:99], v[94:95]
	s_andn2_b64 vcc, exec, s[24:25]
	v_mov_b64_e32 v[96:97], v[92:93]
	s_cbranch_vccnz .LBB0_356
	v_or_b32_e32 v96, s36, v136
	v_ashrrev_i32_e32 v97, 31, v96
	v_lshl_add_u64 v[96:97], v[96:97], 2, s[22:23]
	v_mov_b32_e32 v96, v198
	v_pk_mul_f32 v[98:99], v[94:95], v[96:97] op_sel_hi:[1,0]
	v_pk_mul_f32 v[96:97], v[92:93], v[96:97] op_sel_hi:[1,0]

.LBB0_378:
	s_cmp_eq_u32 s57, 2
	s_mov_b64 s[2:3], -1
	s_cbranch_scc0 .LBB0_397
	v_cndmask_b32_e64 v96, 0, 1, s[24:25]
	v_cmp_ne_u32_e64 s[2:3], 1, v96
	v_mov_b64_e32 v[98:99], v[94:95]
	s_andn2_b64 vcc, exec, s[24:25]
	v_mov_b64_e32 v[96:97], v[92:93]
	s_cbranch_vccnz .LBB0_381
	v_or_b32_e32 v96, s36, v136
	v_ashrrev_i32_e32 v97, 31, v96
	v_lshl_add_u64 v[96:97], v[96:97], 2, s[22:23]
	v_mov_b32_e32 v96, v198
	v_pk_mul_f32 v[98:99], v[94:95], v[96:97] op_sel_hi:[1,0]
	v_pk_mul_f32 v[96:97], v[92:93], v[96:97] op_sel_hi:[1,0]

.LBB0_399:
	v_cndmask_b32_e64 v96, 0, 1, s[24:25]
	v_cmp_ne_u32_e64 s[2:3], 1, v96
	v_mov_b64_e32 v[98:99], v[94:95]
	s_andn2_b64 vcc, exec, s[24:25]
	v_mov_b64_e32 v[96:97], v[92:93]
	s_cbranch_vccnz .LBB0_401
	v_or_b32_e32 v96, s36, v136
	v_ashrrev_i32_e32 v97, 31, v96
	v_lshl_add_u64 v[96:97], v[96:97], 2, s[22:23]
	v_mov_b32_e32 v96, v198
	v_pk_mul_f32 v[98:99], v[94:95], v[96:97] op_sel_hi:[1,0]
	v_pk_mul_f32 v[96:97], v[92:93], v[96:97] op_sel_hi:[1,0]

.LBB0_417:
	v_cndmask_b32_e64 v96, 0, 1, s[24:25]
	v_cmp_ne_u32_e64 s[2:3], 1, v96
	s_andn2_b64 vcc, exec, s[24:25]
	s_cbranch_vccnz .LBB0_419
	v_or_b32_e32 v96, s36, v136
	v_ashrrev_i32_e32 v97, 31, v96
	v_lshl_add_u64 v[96:97], v[96:97], 2, s[22:23]
	v_mov_b32_e32 v96, v198
	v_pk_mul_f32 v[94:95], v[94:95], v[96:97] op_sel_hi:[1,0]
	v_pk_mul_f32 v[92:93], v[92:93], v[96:97] op_sel_hi:[1,0]
.LBB0_419:
	v_pk_mul_f32 v[90:91], v[90:91], s[16:17] op_sel_hi:[1,0]
	s_and_b64 vcc, exec, s[2:3]
	v_pk_mul_f32 v[88:89], v[88:89], s[16:17] op_sel_hi:[1,0]
	ds_write2_b32 v145, v92, v93 offset1:1
	ds_write2_b32 v145, v94, v95 offset0:2 offset1:3
	s_cbranch_vccnz .LBB0_421
	s_ashr_i32 s37, s36, 31
	v_lshl_add_u64 v[92:93], s[36:37], 0, v[136:137]
	v_lshl_add_u64 v[92:93], v[92:93], 2, s[22:23]
	v_mov_b32_e32 v92, v199
	v_pk_mul_f32 v[90:91], v[90:91], v[92:93] op_sel_hi:[1,0]
	v_pk_mul_f32 v[88:89], v[88:89], v[92:93] op_sel_hi:[1,0]
.LBB0_421:
	v_add_u32_e32 v92, v144, v147
	v_pk_mul_f32 v[86:87], v[86:87], s[16:17] op_sel_hi:[1,0]
	s_and_b64 vcc, exec, s[2:3]
	v_pk_mul_f32 v[84:85], v[84:85], s[16:17] op_sel_hi:[1,0]
	ds_write2_b32 v92, v88, v89 offset1:1
	ds_write2_b32 v92, v90, v91 offset0:2 offset1:3
	s_cbranch_vccnz .LBB0_423
	s_ashr_i32 s37, s36, 31
	v_lshl_add_u64 v[88:89], s[36:37], 0, v[136:137]
	v_lshl_add_u64 v[88:89], v[88:89], 2, s[22:23]
	v_mov_b32_e32 v88, v200
	v_pk_mul_f32 v[86:87], v[86:87], v[88:89] op_sel_hi:[1,0]
	v_pk_mul_f32 v[84:85], v[84:85], v[88:89] op_sel_hi:[1,0]
.LBB0_423:
	v_pk_mul_f32 v[82:83], v[82:83], s[16:17] op_sel_hi:[1,0]
	s_and_b64 vcc, exec, s[2:3]
	v_pk_mul_f32 v[80:81], v[80:81], s[16:17] op_sel_hi:[1,0]
	ds_write2_b32 v149, v84, v85 offset1:1
	ds_write2_b32 v149, v86, v87 offset0:2 offset1:3
	s_cbranch_vccnz .LBB0_425
	s_ashr_i32 s37, s36, 31
	v_lshl_add_u64 v[84:85], s[36:37], 0, v[136:137]
	v_lshl_add_u64 v[84:85], v[84:85], 2, s[22:23]
	v_mov_b32_e32 v84, v201
	v_pk_mul_f32 v[82:83], v[82:83], v[84:85] op_sel_hi:[1,0]
	v_pk_mul_f32 v[80:81], v[80:81], v[84:85] op_sel_hi:[1,0]
.LBB0_425:
	v_add_u32_e32 v84, v144, v151
	v_pk_mul_f32 v[78:79], v[78:79], s[16:17] op_sel_hi:[1,0]
	s_and_b64 vcc, exec, s[2:3]
	v_pk_mul_f32 v[76:77], v[76:77], s[16:17] op_sel_hi:[1,0]
	ds_write2_b32 v84, v80, v81 offset1:1
	ds_write2_b32 v84, v82, v83 offset0:2 offset1:3
	s_cbranch_vccnz .LBB0_427
	s_ashr_i32 s37, s36, 31
	v_lshl_add_u64 v[80:81], s[36:37], 0, v[136:137]
	v_lshl_add_u64 v[80:81], v[80:81], 2, s[22:23]
	v_mov_b32_e32 v80, v202
	v_pk_mul_f32 v[78:79], v[78:79], v[80:81] op_sel_hi:[1,0]
	v_pk_mul_f32 v[76:77], v[76:77], v[80:81] op_sel_hi:[1,0]
.LBB0_427:
	v_pk_mul_f32 v[74:75], v[74:75], s[16:17] op_sel_hi:[1,0]
	s_and_b64 vcc, exec, s[2:3]
	v_pk_mul_f32 v[72:73], v[72:73], s[16:17] op_sel_hi:[1,0]
	ds_write2_b32 v152, v76, v77 offset1:1
	ds_write2_b32 v152, v78, v79 offset0:2 offset1:3
	s_cbranch_vccnz .LBB0_429
	s_ashr_i32 s37, s36, 31
	v_lshl_add_u64 v[76:77], s[36:37], 0, v[136:137]
	v_lshl_add_u64 v[76:77], v[76:77], 2, s[22:23]
	v_mov_b32_e32 v76, v203
	v_pk_mul_f32 v[74:75], v[74:75], v[76:77] op_sel_hi:[1,0]
	v_pk_mul_f32 v[72:73], v[72:73], v[76:77] op_sel_hi:[1,0]
.LBB0_429:
	v_add_u32_e32 v76, v144, v153
	v_pk_mul_f32 v[70:71], v[70:71], s[16:17] op_sel_hi:[1,0]
	s_and_b64 vcc, exec, s[2:3]
	v_pk_mul_f32 v[68:69], v[68:69], s[16:17] op_sel_hi:[1,0]
	ds_write2_b32 v76, v72, v73 offset1:1
	ds_write2_b32 v76, v74, v75 offset0:2 offset1:3
	s_cbranch_vccnz .LBB0_431
	s_ashr_i32 s37, s36, 31
	v_lshl_add_u64 v[72:73], s[36:37], 0, v[136:137]
	v_lshl_add_u64 v[72:73], v[72:73], 2, s[22:23]
	v_mov_b32_e32 v72, v204
	v_pk_mul_f32 v[70:71], v[70:71], v[72:73] op_sel_hi:[1,0]
	v_pk_mul_f32 v[68:69], v[68:69], v[72:73] op_sel_hi:[1,0]
.LBB0_431:
	v_pk_mul_f32 v[66:67], v[66:67], s[16:17] op_sel_hi:[1,0]
	v_pk_mul_f32 v[64:65], v[64:65], s[16:17] op_sel_hi:[1,0]
	s_and_b64 vcc, exec, s[24:25]
	ds_write2_b32 v154, v68, v69 offset1:1
	ds_write2_b32 v154, v70, v71 offset0:2 offset1:3
	s_cbranch_vccz .LBB0_838
	s_ashr_i32 s37, s36, 31
	v_lshl_add_u64 v[68:69], s[36:37], 0, v[136:137]
	v_lshl_add_u64 v[68:69], v[68:69], 2, s[22:23]
	v_mov_b32_e32 v68, v205
	v_pk_mul_f32 v[70:71], v[66:67], v[68:69] op_sel_hi:[1,0]
	v_pk_mul_f32 v[68:69], v[64:65], v[68:69] op_sel_hi:[1,0]
	s_cbranch_execnz .LBB0_434

.LBB0_435:
	s_add_i32 s60, s58, 2
	s_sub_i32 s0, -2, s58
	s_max_i32 s0, s60, s0
	s_mul_hi_u32 s1, s0, s56
	s_mul_i32 s2, s1, s4
	s_sub_i32 s0, s0, s2
	s_ashr_i32 s59, s60, 31
	s_add_i32 s2, s1, 1
	s_sub_i32 s3, s0, s4
	s_cmp_ge_u32 s0, s4
	s_cselect_b32 s1, s2, s1
	s_cselect_b32 s0, s3, s0
	s_add_i32 s2, s1, 1
	s_cmp_ge_u32 s0, s4
	s_cselect_b32 s0, s2, s1
	s_xor_b32 s0, s0, s59
	s_sub_i32 s38, s0, s59
	s_lshl_b32 s36, s38, 6
	s_mov_b64 s[0:1], -1
	s_and_b64 vcc, exec, s[34:35]
	s_cbranch_vccz .LBB0_496
	s_cmp_lt_i32 s57, 1
	s_cbranch_scc1 .LBB0_481
	s_cmp_lt_i32 s57, 2
	s_cbranch_scc1 .LBB0_466
	s_cmp_lg_u32 s57, 2
	s_cbranch_scc0 .LBB0_452
	s_waitcnt vmcnt(18)
	v_cndmask_b32_e64 v64, 0, 1, s[24:25]
	v_cmp_ne_u32_e64 s[2:3], 1, v64
	s_andn2_b64 vcc, exec, s[24:25]
	s_cbranch_vccnz .LBB0_876
	v_or_b32_e32 v64, s36, v136
	s_ashr_i32 s37, s36, 31
	v_ashrrev_i32_e32 v65, 31, v64
	v_lshl_add_u64 v[66:67], s[36:37], 0, v[136:137]
	v_lshl_add_u64 v[64:65], v[64:65], 2, s[22:23]
	v_lshl_add_u64 v[66:67], v[66:67], 2, s[22:23]
	v_mov_b32_e32 v64, v198
	s_nop 0
	v_mov_b32_e32 v68, v199
	v_pk_mul_f32 v[70:71], v[62:63], v[64:65] op_sel_hi:[1,0]
	v_pk_mul_f32 v[72:73], v[60:61], v[64:65] op_sel_hi:[1,0]
	v_pk_mul_f32 v[66:67], v[58:59], v[68:69] op_sel_hi:[1,0]
	v_pk_mul_f32 v[64:65], v[56:57], v[68:69] op_sel_hi:[1,0]
	ds_write2_b32 v145, v72, v73 offset1:1
	ds_write2_b32 v145, v70, v71 offset0:2 offset1:3
	s_cbranch_execnz .LBB0_442

.LBB0_442:
	v_add_u32_e32 v68, v144, v147
	s_and_b64 vcc, exec, s[2:3]
	ds_write2_b32 v68, v64, v65 offset1:1
	ds_write2_b32 v68, v66, v67 offset0:2 offset1:3
	s_cbranch_vccnz .LBB0_877
	s_ashr_i32 s37, s36, 31
	v_lshl_add_u64 v[64:65], s[36:37], 0, v[136:137]
	v_lshl_add_u64 v[64:65], v[64:65], 2, s[22:23]
	v_mov_b32_e32 v66, v200
	s_nop 0
	v_mov_b32_e32 v64, v201
	v_pk_mul_f32 v[68:69], v[54:55], v[66:67] op_sel_hi:[1,0]
	v_pk_mul_f32 v[70:71], v[52:53], v[66:67] op_sel_hi:[1,0]
	v_pk_mul_f32 v[66:67], v[50:51], v[64:65] op_sel_hi:[1,0]
	v_pk_mul_f32 v[64:65], v[48:49], v[64:65] op_sel_hi:[1,0]
	ds_write2_b32 v149, v70, v71 offset1:1
	ds_write2_b32 v149, v68, v69 offset0:2 offset1:3
	s_cbranch_execnz .LBB0_445

.LBB0_445:
	v_add_u32_e32 v68, v144, v151
	s_and_b64 vcc, exec, s[2:3]
	ds_write2_b32 v68, v64, v65 offset1:1
	ds_write2_b32 v68, v66, v67 offset0:2 offset1:3
	s_cbranch_vccnz .LBB0_878
	s_ashr_i32 s37, s36, 31
	v_lshl_add_u64 v[64:65], s[36:37], 0, v[136:137]
	v_lshl_add_u64 v[64:65], v[64:65], 2, s[22:23]
	v_mov_b32_e32 v66, v202
	s_nop 0
	v_mov_b32_e32 v64, v203
	v_pk_mul_f32 v[68:69], v[46:47], v[66:67] op_sel_hi:[1,0]
	v_pk_mul_f32 v[70:71], v[44:45], v[66:67] op_sel_hi:[1,0]
	v_pk_mul_f32 v[66:67], v[42:43], v[64:65] op_sel_hi:[1,0]
	v_pk_mul_f32 v[64:65], v[40:41], v[64:65] op_sel_hi:[1,0]
	ds_write2_b32 v152, v70, v71 offset1:1
	ds_write2_b32 v152, v68, v69 offset0:2 offset1:3
	s_cbranch_execnz .LBB0_448

.LBB0_448:
	v_add_u32_e32 v68, v144, v153
	s_and_b64 vcc, exec, s[2:3]
	ds_write2_b32 v68, v64, v65 offset1:1
	ds_write2_b32 v68, v66, v67 offset0:2 offset1:3
	s_cbranch_vccnz .LBB0_879
	s_ashr_i32 s37, s36, 31
	v_lshl_add_u64 v[64:65], s[36:37], 0, v[136:137]
	v_lshl_add_u64 v[64:65], v[64:65], 2, s[22:23]
	v_mov_b32_e32 v66, v204
	s_nop 0
	v_mov_b32_e32 v64, v205
	v_pk_mul_f32 v[68:69], v[38:39], v[66:67] op_sel_hi:[1,0]
	v_pk_mul_f32 v[70:71], v[36:37], v[66:67] op_sel_hi:[1,0]
	v_pk_mul_f32 v[66:67], v[34:35], v[64:65] op_sel_hi:[1,0]
	v_pk_mul_f32 v[64:65], v[32:33], v[64:65] op_sel_hi:[1,0]
	ds_write2_b32 v154, v70, v71 offset1:1
	ds_write2_b32 v154, v68, v69 offset0:2 offset1:3
	s_cbranch_execnz .LBB0_451

.LBB0_452:
	s_and_b64 vcc, exec, s[0:1]
	s_cbranch_vccz .LBB0_823
	s_waitcnt vmcnt(18)
	v_cndmask_b32_e64 v64, 0, 1, s[24:25]
	v_cmp_ne_u32_e64 s[2:3], 1, v64
	s_andn2_b64 vcc, exec, s[24:25]
	s_cbranch_vccnz .LBB0_880
	v_or_b32_e32 v64, s36, v136
	s_ashr_i32 s37, s36, 31
	v_ashrrev_i32_e32 v65, 31, v64
	v_lshl_add_u64 v[66:67], s[36:37], 0, v[136:137]
	v_lshl_add_u64 v[64:65], v[64:65], 2, s[22:23]
	v_lshl_add_u64 v[66:67], v[66:67], 2, s[22:23]
	v_mov_b32_e32 v64, v198
	s_nop 0
	v_mov_b32_e32 v68, v199
	v_pk_mul_f32 v[70:71], v[62:63], v[64:65] op_sel_hi:[1,0]
	v_pk_mul_f32 v[72:73], v[60:61], v[64:65] op_sel_hi:[1,0]
	v_pk_mul_f32 v[66:67], v[58:59], v[68:69] op_sel_hi:[1,0]
	v_pk_mul_f32 v[64:65], v[56:57], v[68:69] op_sel_hi:[1,0]
	ds_write2_b32 v145, v72, v73 offset1:1
	ds_write2_b32 v145, v70, v71 offset0:2 offset1:3
	s_cbranch_execnz .LBB0_456

.LBB0_467:
	s_waitcnt vmcnt(18)
	v_cndmask_b32_e64 v64, 0, 1, s[24:25]
	v_cmp_ne_u32_e64 s[2:3], 1, v64
	s_andn2_b64 vcc, exec, s[24:25]
	s_cbranch_vccnz .LBB0_839
	v_or_b32_e32 v64, s36, v136
	s_ashr_i32 s37, s36, 31
	v_ashrrev_i32_e32 v65, 31, v64
	v_lshl_add_u64 v[66:67], s[36:37], 0, v[136:137]
	v_lshl_add_u64 v[64:65], v[64:65], 2, s[22:23]
	v_lshl_add_u64 v[66:67], v[66:67], 2, s[22:23]
	v_mov_b32_e32 v64, v198
	s_nop 0
	v_mov_b32_e32 v68, v199
	v_pk_mul_f32 v[70:71], v[62:63], v[64:65] op_sel_hi:[1,0]
	v_pk_mul_f32 v[72:73], v[60:61], v[64:65] op_sel_hi:[1,0]
	v_pk_mul_f32 v[66:67], v[58:59], v[68:69] op_sel_hi:[1,0]
	v_pk_mul_f32 v[64:65], v[56:57], v[68:69] op_sel_hi:[1,0]
	ds_write2_b32 v145, v72, v73 offset1:1
	ds_write2_b32 v145, v70, v71 offset0:2 offset1:3
	s_cbranch_execnz .LBB0_470

.LBB0_481:
	s_andn2_b64 vcc, exec, s[0:1]
	s_cbranch_vccnz .LBB0_495
	s_waitcnt vmcnt(18)
	v_cndmask_b32_e64 v64, 0, 1, s[24:25]
	v_cmp_ne_u32_e64 s[2:3], 1, v64
	s_andn2_b64 vcc, exec, s[24:25]
	s_cbranch_vccnz .LBB0_811
	v_or_b32_e32 v64, s36, v136
	s_ashr_i32 s37, s36, 31
	v_ashrrev_i32_e32 v65, 31, v64
	v_lshl_add_u64 v[66:67], s[36:37], 0, v[136:137]
	v_lshl_add_u64 v[64:65], v[64:65], 2, s[22:23]
	v_lshl_add_u64 v[66:67], v[66:67], 2, s[22:23]
	v_mov_b32_e32 v64, v198
	s_nop 0
	v_mov_b32_e32 v68, v199
	v_pk_mul_f32 v[70:71], v[62:63], v[64:65] op_sel_hi:[1,0]
	v_pk_mul_f32 v[72:73], v[60:61], v[64:65] op_sel_hi:[1,0]
	v_pk_mul_f32 v[66:67], v[58:59], v[68:69] op_sel_hi:[1,0]
	v_pk_mul_f32 v[64:65], v[56:57], v[68:69] op_sel_hi:[1,0]
	ds_write2_b32 v145, v72, v73 offset1:1
	ds_write2_b32 v145, v70, v71 offset0:2 offset1:3
	s_cbranch_execnz .LBB0_485

.LBB0_496:
	s_and_b64 vcc, exec, s[0:1]
	s_cbranch_vccz .LBB0_620
	s_waitcnt vmcnt(8)
	v_pk_mul_f32 v[62:63], v[62:63], s[16:17] op_sel_hi:[1,0]
	v_pk_mul_f32 v[60:61], v[60:61], s[16:17] op_sel_hi:[1,0]
	s_cmp_lt_i32 s57, 4
	s_mov_b64 s[0:1], -1
	s_cbranch_scc1 .LBB0_558
	s_cmp_lt_i32 s57, 5
	s_cbranch_scc1 .LBB0_538
	s_cmp_gt_i32 s57, 5
	s_cbranch_scc0 .LBB0_518
	v_cndmask_b32_e64 v64, 0, 1, s[24:25]
	v_cmp_ne_u32_e64 s[2:3], 1, v64
	v_mov_b64_e32 v[66:67], v[62:63]
	s_andn2_b64 vcc, exec, s[24:25]
	v_mov_b64_e32 v[64:65], v[60:61]
	s_cbranch_vccnz .LBB0_502
	v_or_b32_e32 v64, s36, v136
	v_ashrrev_i32_e32 v65, 31, v64
	v_lshl_add_u64 v[64:65], v[64:65], 2, s[22:23]
	v_mov_b32_e32 v64, v198
	v_pk_mul_f32 v[66:67], v[62:63], v[64:65] op_sel_hi:[1,0]
	v_pk_mul_f32 v[64:65], v[60:61], v[64:65] op_sel_hi:[1,0]
.LBB0_502:
	ds_write2_b32 v145, v64, v65 offset1:1
	ds_write2_b32 v145, v66, v67 offset0:2 offset1:3
	v_pk_mul_f32 v[64:65], v[58:59], s[16:17] op_sel_hi:[1,0]
	s_and_b64 vcc, exec, s[2:3]
	v_pk_mul_f32 v[66:67], v[56:57], s[16:17] op_sel_hi:[1,0]
	s_cbranch_vccnz .LBB0_504
	s_ashr_i32 s37, s36, 31
	v_lshl_add_u64 v[68:69], s[36:37], 0, v[136:137]
	v_lshl_add_u64 v[68:69], v[68:69], 2, s[22:23]
	v_mov_b32_e32 v68, v199
	v_pk_mul_f32 v[64:65], v[64:65], v[68:69] op_sel_hi:[1,0]
	v_pk_mul_f32 v[66:67], v[66:67], v[68:69] op_sel_hi:[1,0]
.LBB0_504:
	v_add_u32_e32 v68, v144, v147
	ds_write2_b32 v68, v66, v67 offset1:1
	ds_write2_b32 v68, v64, v65 offset0:2 offset1:3
	v_pk_mul_f32 v[64:65], v[54:55], s[16:17] op_sel_hi:[1,0]
	s_and_b64 vcc, exec, s[2:3]
	v_pk_mul_f32 v[66:67], v[52:53], s[16:17] op_sel_hi:[1,0]
	s_cbranch_vccnz .LBB0_506
	s_ashr_i32 s37, s36, 31
	v_lshl_add_u64 v[68:69], s[36:37], 0, v[136:137]
	v_lshl_add_u64 v[68:69], v[68:69], 2, s[22:23]
	v_mov_b32_e32 v68, v200
	v_pk_mul_f32 v[64:65], v[64:65], v[68:69] op_sel_hi:[1,0]
	v_pk_mul_f32 v[66:67], v[66:67], v[68:69] op_sel_hi:[1,0]
.LBB0_506:
	ds_write2_b32 v149, v66, v67 offset1:1
	ds_write2_b32 v149, v64, v65 offset0:2 offset1:3
	v_pk_mul_f32 v[64:65], v[50:51], s[16:17] op_sel_hi:[1,0]
	s_and_b64 vcc, exec, s[2:3]
	v_pk_mul_f32 v[66:67], v[48:49], s[16:17] op_sel_hi:[1,0]
	s_cbranch_vccnz .LBB0_508
	s_ashr_i32 s37, s36, 31
	v_lshl_add_u64 v[68:69], s[36:37], 0, v[136:137]
	v_lshl_add_u64 v[68:69], v[68:69], 2, s[22:23]
	v_mov_b32_e32 v68, v201
	v_pk_mul_f32 v[64:65], v[64:65], v[68:69] op_sel_hi:[1,0]
	v_pk_mul_f32 v[66:67], v[66:67], v[68:69] op_sel_hi:[1,0]
.LBB0_508:
	v_add_u32_e32 v68, v144, v151
	ds_write2_b32 v68, v66, v67 offset1:1
	ds_write2_b32 v68, v64, v65 offset0:2 offset1:3
	v_pk_mul_f32 v[64:65], v[46:47], s[16:17] op_sel_hi:[1,0]
	s_and_b64 vcc, exec, s[2:3]
	v_pk_mul_f32 v[66:67], v[44:45], s[16:17] op_sel_hi:[1,0]
	s_cbranch_vccnz .LBB0_510
	s_ashr_i32 s37, s36, 31
	v_lshl_add_u64 v[68:69], s[36:37], 0, v[136:137]
	v_lshl_add_u64 v[68:69], v[68:69], 2, s[22:23]
	v_mov_b32_e32 v68, v202
	v_pk_mul_f32 v[64:65], v[64:65], v[68:69] op_sel_hi:[1,0]
	v_pk_mul_f32 v[66:67], v[66:67], v[68:69] op_sel_hi:[1,0]
.LBB0_510:
	ds_write2_b32 v152, v66, v67 offset1:1
	ds_write2_b32 v152, v64, v65 offset0:2 offset1:3
	v_pk_mul_f32 v[64:65], v[42:43], s[16:17] op_sel_hi:[1,0]
	s_and_b64 vcc, exec, s[2:3]
	v_pk_mul_f32 v[66:67], v[40:41], s[16:17] op_sel_hi:[1,0]
	s_cbranch_vccnz .LBB0_512
	s_ashr_i32 s37, s36, 31
	v_lshl_add_u64 v[68:69], s[36:37], 0, v[136:137]
	v_lshl_add_u64 v[68:69], v[68:69], 2, s[22:23]
	v_mov_b32_e32 v68, v203
	v_pk_mul_f32 v[64:65], v[64:65], v[68:69] op_sel_hi:[1,0]
	v_pk_mul_f32 v[66:67], v[66:67], v[68:69] op_sel_hi:[1,0]
.LBB0_512:
	v_add_u32_e32 v68, v144, v153
	ds_write2_b32 v68, v66, v67 offset1:1
	ds_write2_b32 v68, v64, v65 offset0:2 offset1:3
	v_pk_mul_f32 v[64:65], v[38:39], s[16:17] op_sel_hi:[1,0]
	s_and_b64 vcc, exec, s[2:3]
	v_pk_mul_f32 v[66:67], v[36:37], s[16:17] op_sel_hi:[1,0]
	s_cbranch_vccnz .LBB0_514
	s_ashr_i32 s37, s36, 31
	v_lshl_add_u64 v[68:69], s[36:37], 0, v[136:137]
	v_lshl_add_u64 v[68:69], v[68:69], 2, s[22:23]
	v_mov_b32_e32 v68, v204
	v_pk_mul_f32 v[64:65], v[64:65], v[68:69] op_sel_hi:[1,0]
	v_pk_mul_f32 v[66:67], v[66:67], v[68:69] op_sel_hi:[1,0]
.LBB0_514:
	ds_write2_b32 v154, v66, v67 offset1:1
	ds_write2_b32 v154, v64, v65 offset0:2 offset1:3
	v_pk_mul_f32 v[66:67], v[34:35], s[16:17] op_sel_hi:[1,0]
	v_pk_mul_f32 v[64:65], v[32:33], s[16:17] op_sel_hi:[1,0]
	s_and_b64 vcc, exec, s[24:25]
	s_cbranch_vccz .LBB0_884
	s_ashr_i32 s37, s36, 31
	v_lshl_add_u64 v[68:69], s[36:37], 0, v[136:137]
	v_lshl_add_u64 v[68:69], v[68:69], 2, s[22:23]
	v_mov_b32_e32 v68, v205
	v_pk_mul_f32 v[70:71], v[66:67], v[68:69] op_sel_hi:[1,0]
	v_pk_mul_f32 v[68:69], v[64:65], v[68:69] op_sel_hi:[1,0]
	s_cbranch_execnz .LBB0_517

.LBB0_518:
	s_and_b64 vcc, exec, s[0:1]
	s_cbranch_vccz .LBB0_537
	v_cndmask_b32_e64 v64, 0, 1, s[24:25]
	v_cmp_ne_u32_e64 s[2:3], 1, v64
	v_mov_b64_e32 v[66:67], v[62:63]
	s_andn2_b64 vcc, exec, s[24:25]
	v_mov_b64_e32 v[64:65], v[60:61]
	s_cbranch_vccnz .LBB0_521
	v_or_b32_e32 v64, s36, v136
	v_ashrrev_i32_e32 v65, 31, v64
	v_lshl_add_u64 v[64:65], v[64:65], 2, s[22:23]
	v_mov_b32_e32 v64, v198
	v_pk_mul_f32 v[66:67], v[62:63], v[64:65] op_sel_hi:[1,0]
	v_pk_mul_f32 v[64:65], v[60:61], v[64:65] op_sel_hi:[1,0]

.LBB0_538:
	s_andn2_b64 vcc, exec, s[0:1]
	s_cbranch_vccnz .LBB0_557
	v_cndmask_b32_e64 v64, 0, 1, s[24:25]
	v_cmp_ne_u32_e64 s[2:3], 1, v64
	v_mov_b64_e32 v[66:67], v[62:63]
	s_andn2_b64 vcc, exec, s[24:25]
	v_mov_b64_e32 v[64:65], v[60:61]
	s_cbranch_vccnz .LBB0_541
	v_or_b32_e32 v64, s36, v136
	v_ashrrev_i32_e32 v65, 31, v64
	v_lshl_add_u64 v[64:65], v[64:65], 2, s[22:23]
	v_mov_b32_e32 v64, v198
	v_pk_mul_f32 v[66:67], v[62:63], v[64:65] op_sel_hi:[1,0]
	v_pk_mul_f32 v[64:65], v[60:61], v[64:65] op_sel_hi:[1,0]

.LBB0_563:
	s_cmp_eq_u32 s57, 2
	s_mov_b64 s[2:3], -1
	s_cbranch_scc0 .LBB0_582
	v_cndmask_b32_e64 v64, 0, 1, s[24:25]
	v_cmp_ne_u32_e64 s[2:3], 1, v64
	v_mov_b64_e32 v[66:67], v[62:63]
	s_andn2_b64 vcc, exec, s[24:25]
	v_mov_b64_e32 v[64:65], v[60:61]
	s_cbranch_vccnz .LBB0_566
	v_or_b32_e32 v64, s36, v136
	v_ashrrev_i32_e32 v65, 31, v64
	v_lshl_add_u64 v[64:65], v[64:65], 2, s[22:23]
	v_mov_b32_e32 v64, v198
	v_pk_mul_f32 v[66:67], v[62:63], v[64:65] op_sel_hi:[1,0]
	v_pk_mul_f32 v[64:65], v[60:61], v[64:65] op_sel_hi:[1,0]

.LBB0_584:
	v_cndmask_b32_e64 v64, 0, 1, s[24:25]
	v_cmp_ne_u32_e64 s[2:3], 1, v64
	v_mov_b64_e32 v[66:67], v[62:63]
	s_andn2_b64 vcc, exec, s[24:25]
	v_mov_b64_e32 v[64:65], v[60:61]
	s_cbranch_vccnz .LBB0_586
	v_or_b32_e32 v64, s36, v136
	v_ashrrev_i32_e32 v65, 31, v64
	v_lshl_add_u64 v[64:65], v[64:65], 2, s[22:23]
	v_mov_b32_e32 v64, v198
	v_pk_mul_f32 v[66:67], v[62:63], v[64:65] op_sel_hi:[1,0]
	v_pk_mul_f32 v[64:65], v[60:61], v[64:65] op_sel_hi:[1,0]

.LBB0_602:
	v_cndmask_b32_e64 v64, 0, 1, s[24:25]
	v_cmp_ne_u32_e64 s[2:3], 1, v64
	s_andn2_b64 vcc, exec, s[24:25]
	s_cbranch_vccnz .LBB0_604
	v_or_b32_e32 v64, s36, v136
	v_ashrrev_i32_e32 v65, 31, v64
	v_lshl_add_u64 v[64:65], v[64:65], 2, s[22:23]
	v_mov_b32_e32 v64, v198
	v_pk_mul_f32 v[62:63], v[62:63], v[64:65] op_sel_hi:[1,0]
	v_pk_mul_f32 v[60:61], v[60:61], v[64:65] op_sel_hi:[1,0]
.LBB0_604:
	v_pk_mul_f32 v[58:59], v[58:59], s[16:17] op_sel_hi:[1,0]
	s_and_b64 vcc, exec, s[2:3]
	v_pk_mul_f32 v[56:57], v[56:57], s[16:17] op_sel_hi:[1,0]
	ds_write2_b32 v145, v60, v61 offset1:1
	ds_write2_b32 v145, v62, v63 offset0:2 offset1:3
	s_cbranch_vccnz .LBB0_606
	s_ashr_i32 s37, s36, 31
	v_lshl_add_u64 v[60:61], s[36:37], 0, v[136:137]
	v_lshl_add_u64 v[60:61], v[60:61], 2, s[22:23]
	v_mov_b32_e32 v60, v199
	v_pk_mul_f32 v[58:59], v[58:59], v[60:61] op_sel_hi:[1,0]
	v_pk_mul_f32 v[56:57], v[56:57], v[60:61] op_sel_hi:[1,0]
.LBB0_606:
	v_add_u32_e32 v60, v144, v147
	v_pk_mul_f32 v[54:55], v[54:55], s[16:17] op_sel_hi:[1,0]
	s_and_b64 vcc, exec, s[2:3]
	v_pk_mul_f32 v[52:53], v[52:53], s[16:17] op_sel_hi:[1,0]
	ds_write2_b32 v60, v56, v57 offset1:1
	ds_write2_b32 v60, v58, v59 offset0:2 offset1:3
	s_cbranch_vccnz .LBB0_608
	s_ashr_i32 s37, s36, 31
	v_lshl_add_u64 v[56:57], s[36:37], 0, v[136:137]
	v_lshl_add_u64 v[56:57], v[56:57], 2, s[22:23]
	v_mov_b32_e32 v56, v200
	v_pk_mul_f32 v[54:55], v[54:55], v[56:57] op_sel_hi:[1,0]
	v_pk_mul_f32 v[52:53], v[52:53], v[56:57] op_sel_hi:[1,0]
.LBB0_608:
	v_pk_mul_f32 v[50:51], v[50:51], s[16:17] op_sel_hi:[1,0]
	s_and_b64 vcc, exec, s[2:3]
	v_pk_mul_f32 v[48:49], v[48:49], s[16:17] op_sel_hi:[1,0]
	ds_write2_b32 v149, v52, v53 offset1:1
	ds_write2_b32 v149, v54, v55 offset0:2 offset1:3
	s_cbranch_vccnz .LBB0_610
	s_ashr_i32 s37, s36, 31
	v_lshl_add_u64 v[52:53], s[36:37], 0, v[136:137]
	v_lshl_add_u64 v[52:53], v[52:53], 2, s[22:23]
	v_mov_b32_e32 v52, v201
	v_pk_mul_f32 v[50:51], v[50:51], v[52:53] op_sel_hi:[1,0]
	v_pk_mul_f32 v[48:49], v[48:49], v[52:53] op_sel_hi:[1,0]
.LBB0_610:
	v_add_u32_e32 v52, v144, v151
	v_pk_mul_f32 v[46:47], v[46:47], s[16:17] op_sel_hi:[1,0]
	s_and_b64 vcc, exec, s[2:3]
	v_pk_mul_f32 v[44:45], v[44:45], s[16:17] op_sel_hi:[1,0]
	ds_write2_b32 v52, v48, v49 offset1:1
	ds_write2_b32 v52, v50, v51 offset0:2 offset1:3
	s_cbranch_vccnz .LBB0_612
	s_ashr_i32 s37, s36, 31
	v_lshl_add_u64 v[48:49], s[36:37], 0, v[136:137]
	v_lshl_add_u64 v[48:49], v[48:49], 2, s[22:23]
	v_mov_b32_e32 v48, v202
	v_pk_mul_f32 v[46:47], v[46:47], v[48:49] op_sel_hi:[1,0]
	v_pk_mul_f32 v[44:45], v[44:45], v[48:49] op_sel_hi:[1,0]
.LBB0_612:
	v_pk_mul_f32 v[42:43], v[42:43], s[16:17] op_sel_hi:[1,0]
	s_and_b64 vcc, exec, s[2:3]
	v_pk_mul_f32 v[40:41], v[40:41], s[16:17] op_sel_hi:[1,0]
	ds_write2_b32 v152, v44, v45 offset1:1
	ds_write2_b32 v152, v46, v47 offset0:2 offset1:3
	s_cbranch_vccnz .LBB0_614
	s_ashr_i32 s37, s36, 31
	v_lshl_add_u64 v[44:45], s[36:37], 0, v[136:137]
	v_lshl_add_u64 v[44:45], v[44:45], 2, s[22:23]
	v_mov_b32_e32 v44, v203
	v_pk_mul_f32 v[42:43], v[42:43], v[44:45] op_sel_hi:[1,0]
	v_pk_mul_f32 v[40:41], v[40:41], v[44:45] op_sel_hi:[1,0]
.LBB0_614:
	v_add_u32_e32 v44, v144, v153
	v_pk_mul_f32 v[38:39], v[38:39], s[16:17] op_sel_hi:[1,0]
	s_and_b64 vcc, exec, s[2:3]
	v_pk_mul_f32 v[36:37], v[36:37], s[16:17] op_sel_hi:[1,0]
	ds_write2_b32 v44, v40, v41 offset1:1
	ds_write2_b32 v44, v42, v43 offset0:2 offset1:3
	s_cbranch_vccnz .LBB0_616
	s_ashr_i32 s37, s36, 31
	v_lshl_add_u64 v[40:41], s[36:37], 0, v[136:137]
	v_lshl_add_u64 v[40:41], v[40:41], 2, s[22:23]
	v_mov_b32_e32 v40, v204
	v_pk_mul_f32 v[38:39], v[38:39], v[40:41] op_sel_hi:[1,0]
	v_pk_mul_f32 v[36:37], v[36:37], v[40:41] op_sel_hi:[1,0]
.LBB0_616:
	v_pk_mul_f32 v[34:35], v[34:35], s[16:17] op_sel_hi:[1,0]
	v_pk_mul_f32 v[32:33], v[32:33], s[16:17] op_sel_hi:[1,0]
	s_and_b64 vcc, exec, s[24:25]
	ds_write2_b32 v154, v36, v37 offset1:1
	ds_write2_b32 v154, v38, v39 offset0:2 offset1:3
	s_cbranch_vccz .LBB0_845
	s_ashr_i32 s37, s36, 31
	v_lshl_add_u64 v[36:37], s[36:37], 0, v[136:137]
	v_lshl_add_u64 v[36:37], v[36:37], 2, s[22:23]
	v_mov_b32_e32 v36, v205
	v_pk_mul_f32 v[38:39], v[34:35], v[36:37] op_sel_hi:[1,0]
	v_pk_mul_f32 v[36:37], v[32:33], v[36:37] op_sel_hi:[1,0]
	s_cbranch_execnz .LBB0_619

.LBB0_620:
	s_add_i32 s39, s58, 3
	s_sub_i32 s0, -3, s58
	s_max_i32 s0, s39, s0
	s_mul_hi_u32 s1, s0, s56
	s_mul_i32 s2, s1, s4
	s_sub_i32 s0, s0, s2
	s_ashr_i32 s38, s39, 31
	s_add_i32 s2, s1, 1
	s_sub_i32 s3, s0, s4
	s_cmp_ge_u32 s0, s4
	s_cselect_b32 s1, s2, s1
	s_cselect_b32 s0, s3, s0
	s_add_i32 s2, s1, 1
	s_cmp_ge_u32 s0, s4
	s_cselect_b32 s0, s2, s1
	s_xor_b32 s0, s0, s38
	s_sub_i32 s58, s0, s38
	s_lshl_b32 s36, s58, 6
	s_mov_b64 s[0:1], -1
	s_and_b64 vcc, exec, s[34:35]
	s_cbranch_vccz .LBB0_681
	s_cmp_lt_i32 s57, 1
	s_cbranch_scc1 .LBB0_666
	s_cmp_lt_i32 s57, 2
	s_cbranch_scc1 .LBB0_651
	s_cmp_lg_u32 s57, 2
	s_cbranch_scc0 .LBB0_637
	s_waitcnt vmcnt(11)
	v_cndmask_b32_e64 v32, 0, 1, s[24:25]
	v_cmp_ne_u32_e64 s[2:3], 1, v32
	s_andn2_b64 vcc, exec, s[24:25]
	s_cbranch_vccnz .LBB0_887
	v_or_b32_e32 v32, s36, v136
	s_ashr_i32 s37, s36, 31
	v_ashrrev_i32_e32 v33, 31, v32
	v_lshl_add_u64 v[34:35], s[36:37], 0, v[136:137]
	v_lshl_add_u64 v[32:33], v[32:33], 2, s[22:23]
	v_lshl_add_u64 v[34:35], v[34:35], 2, s[22:23]
	v_mov_b32_e32 v32, v198
	s_nop 0
	v_mov_b32_e32 v36, v199
	v_pk_mul_f32 v[38:39], v[30:31], v[32:33] op_sel_hi:[1,0]
	v_pk_mul_f32 v[40:41], v[28:29], v[32:33] op_sel_hi:[1,0]
	v_pk_mul_f32 v[34:35], v[26:27], v[36:37] op_sel_hi:[1,0]
	v_pk_mul_f32 v[32:33], v[24:25], v[36:37] op_sel_hi:[1,0]
	ds_write2_b32 v145, v40, v41 offset1:1
	ds_write2_b32 v145, v38, v39 offset0:2 offset1:3
	s_cbranch_execnz .LBB0_627

.LBB0_627:
	v_add_u32_e32 v36, v144, v147
	s_and_b64 vcc, exec, s[2:3]
	ds_write2_b32 v36, v32, v33 offset1:1
	ds_write2_b32 v36, v34, v35 offset0:2 offset1:3
	s_cbranch_vccnz .LBB0_888
	s_ashr_i32 s37, s36, 31
	v_lshl_add_u64 v[32:33], s[36:37], 0, v[136:137]
	v_lshl_add_u64 v[32:33], v[32:33], 2, s[22:23]
	v_mov_b32_e32 v34, v200
	s_nop 0
	v_mov_b32_e32 v32, v201
	v_pk_mul_f32 v[36:37], v[22:23], v[34:35] op_sel_hi:[1,0]
	v_pk_mul_f32 v[38:39], v[20:21], v[34:35] op_sel_hi:[1,0]
	v_pk_mul_f32 v[34:35], v[18:19], v[32:33] op_sel_hi:[1,0]
	v_pk_mul_f32 v[32:33], v[16:17], v[32:33] op_sel_hi:[1,0]
	ds_write2_b32 v149, v38, v39 offset1:1
	ds_write2_b32 v149, v36, v37 offset0:2 offset1:3
	s_cbranch_execnz .LBB0_630

.LBB0_630:
	v_add_u32_e32 v36, v144, v151
	s_and_b64 vcc, exec, s[2:3]
	ds_write2_b32 v36, v32, v33 offset1:1
	ds_write2_b32 v36, v34, v35 offset0:2 offset1:3
	s_cbranch_vccnz .LBB0_889
	s_ashr_i32 s37, s36, 31
	v_lshl_add_u64 v[32:33], s[36:37], 0, v[136:137]
	v_lshl_add_u64 v[32:33], v[32:33], 2, s[22:23]
	v_mov_b32_e32 v34, v202
	s_nop 0
	v_mov_b32_e32 v32, v203
	v_pk_mul_f32 v[36:37], v[14:15], v[34:35] op_sel_hi:[1,0]
	v_pk_mul_f32 v[38:39], v[12:13], v[34:35] op_sel_hi:[1,0]
	v_pk_mul_f32 v[34:35], v[10:11], v[32:33] op_sel_hi:[1,0]
	v_pk_mul_f32 v[32:33], v[8:9], v[32:33] op_sel_hi:[1,0]
	ds_write2_b32 v152, v38, v39 offset1:1
	ds_write2_b32 v152, v36, v37 offset0:2 offset1:3
	s_cbranch_execnz .LBB0_633

.LBB0_633:
	v_add_u32_e32 v36, v144, v153
	s_and_b64 vcc, exec, s[2:3]
	ds_write2_b32 v36, v32, v33 offset1:1
	ds_write2_b32 v36, v34, v35 offset0:2 offset1:3
	s_cbranch_vccnz .LBB0_890
	s_ashr_i32 s37, s36, 31
	v_lshl_add_u64 v[32:33], s[36:37], 0, v[136:137]
	v_lshl_add_u64 v[32:33], v[32:33], 2, s[22:23]
	v_mov_b32_e32 v34, v204
	s_nop 0
	v_mov_b32_e32 v32, v205
	v_pk_mul_f32 v[36:37], v[6:7], v[34:35] op_sel_hi:[1,0]
	v_pk_mul_f32 v[38:39], v[4:5], v[34:35] op_sel_hi:[1,0]
	v_pk_mul_f32 v[34:35], v[2:3], v[32:33] op_sel_hi:[1,0]
	v_pk_mul_f32 v[32:33], v[0:1], v[32:33] op_sel_hi:[1,0]
	ds_write2_b32 v154, v38, v39 offset1:1
	ds_write2_b32 v154, v36, v37 offset0:2 offset1:3
	s_cbranch_execnz .LBB0_636

.LBB0_637:
	s_and_b64 vcc, exec, s[0:1]
	s_cbranch_vccz .LBB0_824
	s_waitcnt vmcnt(11)
	v_cndmask_b32_e64 v32, 0, 1, s[24:25]
	v_cmp_ne_u32_e64 s[2:3], 1, v32
	s_andn2_b64 vcc, exec, s[24:25]
	s_cbranch_vccnz .LBB0_891
	v_or_b32_e32 v32, s36, v136
	s_ashr_i32 s37, s36, 31
	v_ashrrev_i32_e32 v33, 31, v32
	v_lshl_add_u64 v[34:35], s[36:37], 0, v[136:137]
	v_lshl_add_u64 v[32:33], v[32:33], 2, s[22:23]
	v_lshl_add_u64 v[34:35], v[34:35], 2, s[22:23]
	v_mov_b32_e32 v32, v198
	s_nop 0
	v_mov_b32_e32 v36, v199
	v_pk_mul_f32 v[38:39], v[30:31], v[32:33] op_sel_hi:[1,0]
	v_pk_mul_f32 v[40:41], v[28:29], v[32:33] op_sel_hi:[1,0]
	v_pk_mul_f32 v[34:35], v[26:27], v[36:37] op_sel_hi:[1,0]
	v_pk_mul_f32 v[32:33], v[24:25], v[36:37] op_sel_hi:[1,0]
	ds_write2_b32 v145, v40, v41 offset1:1
	ds_write2_b32 v145, v38, v39 offset0:2 offset1:3
	s_cbranch_execnz .LBB0_641

.LBB0_652:
	s_waitcnt vmcnt(11)
	v_cndmask_b32_e64 v32, 0, 1, s[24:25]
	v_cmp_ne_u32_e64 s[2:3], 1, v32
	s_andn2_b64 vcc, exec, s[24:25]
	s_cbranch_vccnz .LBB0_846
	v_or_b32_e32 v32, s36, v136
	s_ashr_i32 s37, s36, 31
	v_ashrrev_i32_e32 v33, 31, v32
	v_lshl_add_u64 v[34:35], s[36:37], 0, v[136:137]
	v_lshl_add_u64 v[32:33], v[32:33], 2, s[22:23]
	v_lshl_add_u64 v[34:35], v[34:35], 2, s[22:23]
	v_mov_b32_e32 v32, v198
	s_nop 0
	v_mov_b32_e32 v36, v199
	v_pk_mul_f32 v[38:39], v[30:31], v[32:33] op_sel_hi:[1,0]
	v_pk_mul_f32 v[40:41], v[28:29], v[32:33] op_sel_hi:[1,0]
	v_pk_mul_f32 v[34:35], v[26:27], v[36:37] op_sel_hi:[1,0]
	v_pk_mul_f32 v[32:33], v[24:25], v[36:37] op_sel_hi:[1,0]
	ds_write2_b32 v145, v40, v41 offset1:1
	ds_write2_b32 v145, v38, v39 offset0:2 offset1:3
	s_cbranch_execnz .LBB0_655

.LBB0_666:
	s_andn2_b64 vcc, exec, s[0:1]
	s_cbranch_vccnz .LBB0_680
	s_waitcnt vmcnt(11)
	v_cndmask_b32_e64 v32, 0, 1, s[24:25]
	v_cmp_ne_u32_e64 s[2:3], 1, v32
	s_andn2_b64 vcc, exec, s[24:25]
	s_cbranch_vccnz .LBB0_815
	v_or_b32_e32 v32, s36, v136
	s_ashr_i32 s37, s36, 31
	v_ashrrev_i32_e32 v33, 31, v32
	v_lshl_add_u64 v[34:35], s[36:37], 0, v[136:137]
	v_lshl_add_u64 v[32:33], v[32:33], 2, s[22:23]
	v_lshl_add_u64 v[34:35], v[34:35], 2, s[22:23]
	v_mov_b32_e32 v32, v198
	s_nop 0
	v_mov_b32_e32 v36, v199
	v_pk_mul_f32 v[38:39], v[30:31], v[32:33] op_sel_hi:[1,0]
	v_pk_mul_f32 v[40:41], v[28:29], v[32:33] op_sel_hi:[1,0]
	v_pk_mul_f32 v[34:35], v[26:27], v[36:37] op_sel_hi:[1,0]
	v_pk_mul_f32 v[32:33], v[24:25], v[36:37] op_sel_hi:[1,0]
	ds_write2_b32 v145, v40, v41 offset1:1
	ds_write2_b32 v145, v38, v39 offset0:2 offset1:3
	s_cbranch_execnz .LBB0_670

.LBB0_681:
	s_and_b64 vcc, exec, s[0:1]
	s_cbranch_vccz .LBB0_17
	s_waitcnt vmcnt(7)
	v_pk_mul_f32 v[30:31], v[30:31], s[16:17] op_sel_hi:[1,0]
	v_pk_mul_f32 v[28:29], v[28:29], s[16:17] op_sel_hi:[1,0]
	s_cmp_lt_i32 s57, 4
	s_mov_b64 s[0:1], -1
	s_cbranch_scc1 .LBB0_743
	s_cmp_lt_i32 s57, 5
	s_cbranch_scc1 .LBB0_723
	s_cmp_gt_i32 s57, 5
	s_cbranch_scc0 .LBB0_703
	v_cndmask_b32_e64 v32, 0, 1, s[24:25]
	v_cmp_ne_u32_e64 s[2:3], 1, v32
	v_mov_b64_e32 v[34:35], v[30:31]
	s_andn2_b64 vcc, exec, s[24:25]
	v_mov_b64_e32 v[32:33], v[28:29]
	s_cbranch_vccnz .LBB0_687
	v_or_b32_e32 v32, s36, v136
	v_ashrrev_i32_e32 v33, 31, v32
	v_lshl_add_u64 v[32:33], v[32:33], 2, s[22:23]
	v_mov_b32_e32 v32, v198
	v_pk_mul_f32 v[34:35], v[30:31], v[32:33] op_sel_hi:[1,0]
	v_pk_mul_f32 v[32:33], v[28:29], v[32:33] op_sel_hi:[1,0]
.LBB0_687:
	ds_write2_b32 v145, v32, v33 offset1:1
	ds_write2_b32 v145, v34, v35 offset0:2 offset1:3
	s_waitcnt vmcnt(2)
	v_pk_mul_f32 v[32:33], v[26:27], s[16:17] op_sel_hi:[1,0]
	s_and_b64 vcc, exec, s[2:3]
	v_pk_mul_f32 v[34:35], v[24:25], s[16:17] op_sel_hi:[1,0]
	s_cbranch_vccnz .LBB0_689
	s_ashr_i32 s37, s36, 31
	v_lshl_add_u64 v[36:37], s[36:37], 0, v[136:137]
	v_lshl_add_u64 v[36:37], v[36:37], 2, s[22:23]
	v_mov_b32_e32 v36, v199
	v_pk_mul_f32 v[32:33], v[32:33], v[36:37] op_sel_hi:[1,0]
	v_pk_mul_f32 v[34:35], v[34:35], v[36:37] op_sel_hi:[1,0]
.LBB0_689:
	v_add_u32_e32 v36, v144, v147
	ds_write2_b32 v36, v34, v35 offset1:1
	ds_write2_b32 v36, v32, v33 offset0:2 offset1:3
	v_pk_mul_f32 v[32:33], v[22:23], s[16:17] op_sel_hi:[1,0]
	s_and_b64 vcc, exec, s[2:3]
	v_pk_mul_f32 v[34:35], v[20:21], s[16:17] op_sel_hi:[1,0]
	s_cbranch_vccnz .LBB0_691
	s_ashr_i32 s37, s36, 31
	v_lshl_add_u64 v[36:37], s[36:37], 0, v[136:137]
	v_lshl_add_u64 v[36:37], v[36:37], 2, s[22:23]
	v_mov_b32_e32 v36, v200
	v_pk_mul_f32 v[32:33], v[32:33], v[36:37] op_sel_hi:[1,0]
	v_pk_mul_f32 v[34:35], v[34:35], v[36:37] op_sel_hi:[1,0]
.LBB0_691:
	ds_write2_b32 v149, v34, v35 offset1:1
	ds_write2_b32 v149, v32, v33 offset0:2 offset1:3
	v_pk_mul_f32 v[32:33], v[18:19], s[16:17] op_sel_hi:[1,0]
	s_and_b64 vcc, exec, s[2:3]
	v_pk_mul_f32 v[34:35], v[16:17], s[16:17] op_sel_hi:[1,0]
	s_cbranch_vccnz .LBB0_693
	s_ashr_i32 s37, s36, 31
	v_lshl_add_u64 v[36:37], s[36:37], 0, v[136:137]
	v_lshl_add_u64 v[36:37], v[36:37], 2, s[22:23]
	v_mov_b32_e32 v36, v201
	v_pk_mul_f32 v[32:33], v[32:33], v[36:37] op_sel_hi:[1,0]
	v_pk_mul_f32 v[34:35], v[34:35], v[36:37] op_sel_hi:[1,0]
.LBB0_693:
	v_add_u32_e32 v36, v144, v151
	ds_write2_b32 v36, v34, v35 offset1:1
	ds_write2_b32 v36, v32, v33 offset0:2 offset1:3
	v_pk_mul_f32 v[32:33], v[14:15], s[16:17] op_sel_hi:[1,0]
	s_and_b64 vcc, exec, s[2:3]
	v_pk_mul_f32 v[34:35], v[12:13], s[16:17] op_sel_hi:[1,0]
	s_cbranch_vccnz .LBB0_695
	s_ashr_i32 s37, s36, 31
	v_lshl_add_u64 v[36:37], s[36:37], 0, v[136:137]
	v_lshl_add_u64 v[36:37], v[36:37], 2, s[22:23]
	v_mov_b32_e32 v36, v202
	v_pk_mul_f32 v[32:33], v[32:33], v[36:37] op_sel_hi:[1,0]
	v_pk_mul_f32 v[34:35], v[34:35], v[36:37] op_sel_hi:[1,0]
.LBB0_695:
	ds_write2_b32 v152, v34, v35 offset1:1
	ds_write2_b32 v152, v32, v33 offset0:2 offset1:3
	v_pk_mul_f32 v[32:33], v[10:11], s[16:17] op_sel_hi:[1,0]
	s_and_b64 vcc, exec, s[2:3]
	v_pk_mul_f32 v[34:35], v[8:9], s[16:17] op_sel_hi:[1,0]
	s_cbranch_vccnz .LBB0_697
	s_ashr_i32 s37, s36, 31
	v_lshl_add_u64 v[36:37], s[36:37], 0, v[136:137]
	v_lshl_add_u64 v[36:37], v[36:37], 2, s[22:23]
	v_mov_b32_e32 v36, v203
	v_pk_mul_f32 v[32:33], v[32:33], v[36:37] op_sel_hi:[1,0]
	v_pk_mul_f32 v[34:35], v[34:35], v[36:37] op_sel_hi:[1,0]
.LBB0_697:
	v_add_u32_e32 v36, v144, v153
	ds_write2_b32 v36, v34, v35 offset1:1
	ds_write2_b32 v36, v32, v33 offset0:2 offset1:3
	s_waitcnt vmcnt(1)
	v_pk_mul_f32 v[32:33], v[6:7], s[16:17] op_sel_hi:[1,0]
	s_and_b64 vcc, exec, s[2:3]
	v_pk_mul_f32 v[34:35], v[4:5], s[16:17] op_sel_hi:[1,0]
	s_cbranch_vccnz .LBB0_699
	s_ashr_i32 s37, s36, 31
	v_lshl_add_u64 v[36:37], s[36:37], 0, v[136:137]
	v_lshl_add_u64 v[36:37], v[36:37], 2, s[22:23]
	v_mov_b32_e32 v36, v204
	v_pk_mul_f32 v[32:33], v[32:33], v[36:37] op_sel_hi:[1,0]
	v_pk_mul_f32 v[34:35], v[34:35], v[36:37] op_sel_hi:[1,0]
.LBB0_699:
	ds_write2_b32 v154, v34, v35 offset1:1
	ds_write2_b32 v154, v32, v33 offset0:2 offset1:3
	s_waitcnt vmcnt(0)
	v_pk_mul_f32 v[34:35], v[2:3], s[16:17] op_sel_hi:[1,0]
	v_pk_mul_f32 v[32:33], v[0:1], s[16:17] op_sel_hi:[1,0]
	s_and_b64 vcc, exec, s[24:25]
	s_cbranch_vccz .LBB0_895
	s_ashr_i32 s37, s36, 31
	v_lshl_add_u64 v[36:37], s[36:37], 0, v[136:137]
	v_lshl_add_u64 v[36:37], v[36:37], 2, s[22:23]
	v_mov_b32_e32 v36, v205
	v_pk_mul_f32 v[38:39], v[34:35], v[36:37] op_sel_hi:[1,0]
	v_pk_mul_f32 v[36:37], v[32:33], v[36:37] op_sel_hi:[1,0]
	s_cbranch_execnz .LBB0_702

.LBB0_703:
	s_and_b64 vcc, exec, s[0:1]
	s_cbranch_vccz .LBB0_722
	v_cndmask_b32_e64 v32, 0, 1, s[24:25]
	v_cmp_ne_u32_e64 s[2:3], 1, v32
	v_mov_b64_e32 v[34:35], v[30:31]
	s_andn2_b64 vcc, exec, s[24:25]
	v_mov_b64_e32 v[32:33], v[28:29]
	s_cbranch_vccnz .LBB0_706
	v_or_b32_e32 v32, s36, v136
	v_ashrrev_i32_e32 v33, 31, v32
	v_lshl_add_u64 v[32:33], v[32:33], 2, s[22:23]
	v_mov_b32_e32 v32, v198
	v_pk_mul_f32 v[34:35], v[30:31], v[32:33] op_sel_hi:[1,0]
	v_pk_mul_f32 v[32:33], v[28:29], v[32:33] op_sel_hi:[1,0]

.LBB0_723:
	s_andn2_b64 vcc, exec, s[0:1]
	s_cbranch_vccnz .LBB0_742
	v_cndmask_b32_e64 v32, 0, 1, s[24:25]
	v_cmp_ne_u32_e64 s[2:3], 1, v32
	v_mov_b64_e32 v[34:35], v[30:31]
	s_andn2_b64 vcc, exec, s[24:25]
	v_mov_b64_e32 v[32:33], v[28:29]
	s_cbranch_vccnz .LBB0_726
	v_or_b32_e32 v32, s36, v136
	v_ashrrev_i32_e32 v33, 31, v32
	v_lshl_add_u64 v[32:33], v[32:33], 2, s[22:23]
	v_mov_b32_e32 v32, v198
	v_pk_mul_f32 v[34:35], v[30:31], v[32:33] op_sel_hi:[1,0]
	v_pk_mul_f32 v[32:33], v[28:29], v[32:33] op_sel_hi:[1,0]

.LBB0_748:
	s_cmp_eq_u32 s57, 2
	s_mov_b64 s[2:3], -1
	s_cbranch_scc0 .LBB0_767
	v_cndmask_b32_e64 v32, 0, 1, s[24:25]
	v_cmp_ne_u32_e64 s[2:3], 1, v32
	v_mov_b64_e32 v[34:35], v[30:31]
	s_andn2_b64 vcc, exec, s[24:25]
	v_mov_b64_e32 v[32:33], v[28:29]
	s_cbranch_vccnz .LBB0_751
	v_or_b32_e32 v32, s36, v136
	v_ashrrev_i32_e32 v33, 31, v32
	v_lshl_add_u64 v[32:33], v[32:33], 2, s[22:23]
	v_mov_b32_e32 v32, v198
	v_pk_mul_f32 v[34:35], v[30:31], v[32:33] op_sel_hi:[1,0]
	v_pk_mul_f32 v[32:33], v[28:29], v[32:33] op_sel_hi:[1,0]

.LBB0_769:
	v_mov_b64_e32 v[34:35], v[30:31]
	s_and_b64 vcc, exec, s[2:3]
	v_mov_b64_e32 v[32:33], v[28:29]
	s_cbranch_vccnz .LBB0_771
	v_or_b32_e32 v32, s36, v136
	v_ashrrev_i32_e32 v33, 31, v32
	v_lshl_add_u64 v[32:33], v[32:33], 2, s[22:23]
	v_mov_b32_e32 v32, v198
	v_pk_mul_f32 v[34:35], v[30:31], v[32:33] op_sel_hi:[1,0]
	v_pk_mul_f32 v[32:33], v[28:29], v[32:33] op_sel_hi:[1,0]

.LBB0_787:
	s_and_b64 vcc, exec, s[2:3]
	s_cbranch_vccnz .LBB0_789
	v_or_b32_e32 v32, s36, v136
	v_ashrrev_i32_e32 v33, 31, v32
	v_lshl_add_u64 v[32:33], v[32:33], 2, s[22:23]
	v_mov_b32_e32 v32, v198
	v_pk_mul_f32 v[30:31], v[30:31], v[32:33] op_sel_hi:[1,0]
	v_pk_mul_f32 v[28:29], v[28:29], v[32:33] op_sel_hi:[1,0]
.LBB0_789:
	s_waitcnt vmcnt(2)
	v_pk_mul_f32 v[26:27], v[26:27], s[16:17] op_sel_hi:[1,0]
	s_and_b64 vcc, exec, s[2:3]
	v_pk_mul_f32 v[24:25], v[24:25], s[16:17] op_sel_hi:[1,0]
	ds_write2_b32 v145, v28, v29 offset1:1
	ds_write2_b32 v145, v30, v31 offset0:2 offset1:3
	s_cbranch_vccnz .LBB0_791
	s_ashr_i32 s37, s36, 31
	v_lshl_add_u64 v[28:29], s[36:37], 0, v[136:137]
	v_lshl_add_u64 v[28:29], v[28:29], 2, s[22:23]
	v_mov_b32_e32 v28, v199
	v_pk_mul_f32 v[26:27], v[26:27], v[28:29] op_sel_hi:[1,0]
	v_pk_mul_f32 v[24:25], v[24:25], v[28:29] op_sel_hi:[1,0]
.LBB0_791:
	v_add_u32_e32 v28, v144, v147
	v_pk_mul_f32 v[22:23], v[22:23], s[16:17] op_sel_hi:[1,0]
	s_and_b64 vcc, exec, s[2:3]
	v_pk_mul_f32 v[20:21], v[20:21], s[16:17] op_sel_hi:[1,0]
	ds_write2_b32 v28, v24, v25 offset1:1
	ds_write2_b32 v28, v26, v27 offset0:2 offset1:3
	s_cbranch_vccnz .LBB0_793
	s_ashr_i32 s37, s36, 31
	v_lshl_add_u64 v[24:25], s[36:37], 0, v[136:137]
	v_lshl_add_u64 v[24:25], v[24:25], 2, s[22:23]
	v_mov_b32_e32 v24, v200
	v_pk_mul_f32 v[22:23], v[22:23], v[24:25] op_sel_hi:[1,0]
	v_pk_mul_f32 v[20:21], v[20:21], v[24:25] op_sel_hi:[1,0]
.LBB0_793:
	v_pk_mul_f32 v[18:19], v[18:19], s[16:17] op_sel_hi:[1,0]
	s_and_b64 vcc, exec, s[2:3]
	v_pk_mul_f32 v[16:17], v[16:17], s[16:17] op_sel_hi:[1,0]
	ds_write2_b32 v149, v20, v21 offset1:1
	ds_write2_b32 v149, v22, v23 offset0:2 offset1:3
	s_cbranch_vccnz .LBB0_795
	s_ashr_i32 s37, s36, 31
	v_lshl_add_u64 v[20:21], s[36:37], 0, v[136:137]
	v_lshl_add_u64 v[20:21], v[20:21], 2, s[22:23]
	v_mov_b32_e32 v20, v201
	v_pk_mul_f32 v[18:19], v[18:19], v[20:21] op_sel_hi:[1,0]
	v_pk_mul_f32 v[16:17], v[16:17], v[20:21] op_sel_hi:[1,0]
.LBB0_795:
	v_add_u32_e32 v20, v144, v151
	v_pk_mul_f32 v[14:15], v[14:15], s[16:17] op_sel_hi:[1,0]
	s_and_b64 vcc, exec, s[2:3]
	v_pk_mul_f32 v[12:13], v[12:13], s[16:17] op_sel_hi:[1,0]
	ds_write2_b32 v20, v16, v17 offset1:1
	ds_write2_b32 v20, v18, v19 offset0:2 offset1:3
	s_cbranch_vccnz .LBB0_797
	s_ashr_i32 s37, s36, 31
	v_lshl_add_u64 v[16:17], s[36:37], 0, v[136:137]
	v_lshl_add_u64 v[16:17], v[16:17], 2, s[22:23]
	v_mov_b32_e32 v16, v202
	v_pk_mul_f32 v[14:15], v[14:15], v[16:17] op_sel_hi:[1,0]
	v_pk_mul_f32 v[12:13], v[12:13], v[16:17] op_sel_hi:[1,0]
.LBB0_797:
	v_pk_mul_f32 v[10:11], v[10:11], s[16:17] op_sel_hi:[1,0]
	s_and_b64 vcc, exec, s[2:3]
	v_pk_mul_f32 v[8:9], v[8:9], s[16:17] op_sel_hi:[1,0]
	ds_write2_b32 v152, v12, v13 offset1:1
	ds_write2_b32 v152, v14, v15 offset0:2 offset1:3
	s_cbranch_vccnz .LBB0_799
	s_ashr_i32 s37, s36, 31
	v_lshl_add_u64 v[12:13], s[36:37], 0, v[136:137]
	v_lshl_add_u64 v[12:13], v[12:13], 2, s[22:23]
	v_mov_b32_e32 v12, v203
	v_pk_mul_f32 v[10:11], v[10:11], v[12:13] op_sel_hi:[1,0]
	v_pk_mul_f32 v[8:9], v[8:9], v[12:13] op_sel_hi:[1,0]
.LBB0_799:
	v_add_u32_e32 v12, v144, v153
	s_waitcnt vmcnt(1)
	v_pk_mul_f32 v[6:7], v[6:7], s[16:17] op_sel_hi:[1,0]
	s_and_b64 vcc, exec, s[2:3]
	v_pk_mul_f32 v[4:5], v[4:5], s[16:17] op_sel_hi:[1,0]
	ds_write2_b32 v12, v8, v9 offset1:1
	ds_write2_b32 v12, v10, v11 offset0:2 offset1:3
	s_cbranch_vccnz .LBB0_801
	s_ashr_i32 s37, s36, 31
	v_lshl_add_u64 v[8:9], s[36:37], 0, v[136:137]
	v_lshl_add_u64 v[8:9], v[8:9], 2, s[22:23]
	v_mov_b32_e32 v8, v204
	v_pk_mul_f32 v[6:7], v[6:7], v[8:9] op_sel_hi:[1,0]
	v_pk_mul_f32 v[4:5], v[4:5], v[8:9] op_sel_hi:[1,0]
.LBB0_801:
	s_waitcnt vmcnt(0)
	v_pk_mul_f32 v[2:3], v[2:3], s[16:17] op_sel_hi:[1,0]
	v_pk_mul_f32 v[0:1], v[0:1], s[16:17] op_sel_hi:[1,0]
	s_and_b64 vcc, exec, s[24:25]
	ds_write2_b32 v154, v4, v5 offset1:1
	ds_write2_b32 v154, v6, v7 offset0:2 offset1:3
	s_cbranch_vccz .LBB0_852
	s_ashr_i32 s37, s36, 31
	v_lshl_add_u64 v[4:5], s[36:37], 0, v[136:137]
	v_lshl_add_u64 v[4:5], v[4:5], 2, s[22:23]
	v_mov_b32_e32 v4, v205
	v_pk_mul_f32 v[6:7], v[2:3], v[4:5] op_sel_hi:[1,0]
	v_pk_mul_f32 v[4:5], v[0:1], v[4:5] op_sel_hi:[1,0]
	s_cbranch_execnz .LBB0_16
	s_branch .LBB0_853
